# speedup vs baseline: 1.0189x; 1.0189x over previous
.LBB0_3:
	s_load_dwordx2 s[4:5], s[0:1], 0x18
	s_cmpk_gt_u32 s2, 0x1ff
	s_mov_b64 s[6:7], -1
	s_cbranch_scc0 .LBB0_12
	s_cmpk_lt_u32 s2, 0x220
	s_cbranch_scc0 .LBB0_8
	v_lshl_or_b32 v1, s2, 8, v0
	v_lshrrev_b32_e32 v4, 3, v0
	v_and_b32_e32 v5, 15, v4
	v_bfe_u32 v4, v0, 7, 1
	v_lshlrev_b32_e32 v4, 3, v4
	v_sub_u32_e32 v4, v5, v4
	v_add_u32_e32 v2, 0xfffe0000, v1
	v_cmp_gt_u32_e32 vcc, 6, v4
	v_mov_b32_e32 v3, 0
	v_mov_b32_e32 v1, 0
	s_and_saveexec_b64 s[6:7], vcc
	s_cbranch_execz .LBB0_7
	s_load_dwordx2 s[10:11], s[0:1], 0x20
	v_lshrrev_b32_e32 v1, 5, v2
	v_lshlrev_b32_e32 v5, 1, v0
	v_lshrrev_b32_e32 v6, 6, v2
	v_and_b32_e32 v7, 3, v0
	v_and_b32_e32 v1, 0x7fffff0, v1
	v_and_b32_e32 v6, 4, v6
	v_and_or_b32 v5, v5, 8, v7
	v_or3_b32 v1, v5, v1, v6
	v_mad_u64_u32 v[4:5], s[12:13], v1, 6, v[4:5]
	v_mov_b32_e32 v5, 0
	s_waitcnt lgkmcnt(0)
	v_lshl_add_u64 v[4:5], v[4:5], 2, s[10:11]
	global_load_dword v1, v[4:5], off
	s_waitcnt vmcnt(0)
	v_cvt_f16_f32_e32 v1, v1

.LBB1_20:
	s_add_u32 s45, s12, 0x200000
	s_addc_u32 s46, s13, 0
	s_cmpk_lt_u32 s21, 0x100
	s_cselect_b64 s[22:23], -1, 0
	s_or_b64 s[26:27], s[16:17], s[22:23]
	s_and_b64 s[0:1], s[26:27], exec
	s_cselect_b32 s31, s13, s46
	s_cselect_b32 s34, s12, s45
	s_add_u32 s0, s12, 0x400000
	s_addc_u32 s1, s13, 0
	s_lshl_b32 s24, s9, 6
	s_ashr_i32 s25, s24, 31
	s_lshl_b64 s[24:25], s[24:25], 4
	s_add_u32 s34, s34, s24
	s_addc_u32 s35, s31, s25
	s_lshl_b32 s24, s42, 4
	s_and_b64 s[26:27], s[26:27], exec
	s_cselect_b32 s9, s46, s13
	s_cselect_b32 s25, s45, s12
	s_and_b64 s[26:27], exec, s[16:17]
	v_mul_u32_u24_e32 v20, 0x2aab, v0
	s_cselect_b32 s8, s8, s24
	v_lshrrev_b32_e32 v156, 16, v20
	s_add_i32 s4, s4, s8
	s_lshl_b32 s8, s3, 2
	v_mul_lo_u16_e32 v20, 6, v156
	s_and_b32 s47, s8, 12
	v_sub_u16_e32 v20, v0, v20
	s_or_b32 s4, s4, s47
	v_lshlrev_b32_e32 v20, 2, v20
	v_lshl_or_b32 v24, s4, 6, v199
	global_load_dword v176, v20, s[14:15]
	v_mov_b32_e32 v20, s25
	v_mov_b32_e32 v21, s9
	v_ashrrev_i32_e32 v25, 31, v24
	v_mov_b32_e32 v167, 0
	v_lshlrev_b32_e32 v166, 4, v199
	v_lshl_add_u64 v[20:21], v[24:25], 4, v[20:21]
	s_mov_b32 s5, 0
	v_lshl_add_u64 v[18:19], s[34:35], 0, v[166:167]
	global_load_dwordx4 v[146:149], v[20:21], off
	global_load_dwordx4 v[138:141], v[20:21], off offset:1024
	global_load_dwordx4 v[24:27], v166, s[34:35]
	s_lshl_b32 s4, s20, 4
	v_lshl_add_u64 v[18:19], v[18:19], 0, s[4:5]
	global_load_dwordx4 v[28:31], v[18:19], off
	global_load_dwordx4 v[150:153], v[20:21], off offset:2048
	global_load_dwordx4 v[142:145], v[20:21], off offset:3072
	s_lshl_b32 s9, s21, 4
	s_and_b32 s8, s21, 64
	s_and_b32 s9, s9, 0xfffff800
	s_or_b32 s8, s8, s9
	v_or_b32_e32 v34, s8, v199
	v_lshl_add_u64 v[32:33], v[18:19], 0, s[4:5]
	v_ashrrev_i32_e32 v35, 31, v34
	v_or_b32_e32 v38, 0x80, v34
	global_load_dwordx4 v[18:21], v[32:33], off
	v_lshl_add_u64 v[32:33], v[32:33], 0, s[4:5]
	v_lshl_add_u64 v[36:37], v[34:35], 4, s[0:1]
	v_ashrrev_i32_e32 v39, 31, v38
	global_load_dwordx4 v[62:65], v[32:33], off
	v_lshl_add_u64 v[38:39], v[38:39], 4, s[0:1]
	global_load_dwordx4 v[122:125], v[36:37], off
	global_load_dwordx4 v[98:101], v[38:39], off
	v_or_b32_e32 v36, 0x100, v34
	v_ashrrev_i32_e32 v37, 31, v36
	v_or_b32_e32 v38, 0x180, v34
	v_lshl_add_u64 v[36:37], v[36:37], 4, s[0:1]
	v_ashrrev_i32_e32 v39, 31, v38
	v_lshl_add_u64 v[38:39], v[38:39], 4, s[0:1]
	global_load_dwordx4 v[114:117], v[36:37], off
	global_load_dwordx4 v[86:89], v[38:39], off
	v_or_b32_e32 v36, 0x200, v34
	v_ashrrev_i32_e32 v37, 31, v36
	v_or_b32_e32 v38, 0x280, v34
	v_lshl_add_u64 v[36:37], v[36:37], 4, s[0:1]
	v_ashrrev_i32_e32 v39, 31, v38
	v_lshl_add_u64 v[38:39], v[38:39], 4, s[0:1]
	global_load_dwordx4 v[126:129], v[36:37], off
	global_load_dwordx4 v[90:93], v[38:39], off
	v_or_b32_e32 v36, 0x300, v34
	v_ashrrev_i32_e32 v37, 31, v36
	v_or_b32_e32 v38, 0x380, v34
	v_lshl_add_u64 v[36:37], v[36:37], 4, s[0:1]
	v_ashrrev_i32_e32 v39, 31, v38
	v_lshl_add_u64 v[38:39], v[38:39], 4, s[0:1]
	global_load_dwordx4 v[118:121], v[36:37], off
	global_load_dwordx4 v[78:81], v[38:39], off
	v_or_b32_e32 v36, 0x400, v34
	v_ashrrev_i32_e32 v37, 31, v36
	v_or_b32_e32 v38, 0x480, v34
	v_lshl_add_u64 v[36:37], v[36:37], 4, s[0:1]
	v_ashrrev_i32_e32 v39, 31, v38
	v_lshl_add_u64 v[38:39], v[38:39], 4, s[0:1]
	global_load_dwordx4 v[102:105], v[36:37], off
	global_load_dwordx4 v[74:77], v[38:39], off
	v_or_b32_e32 v36, 0x500, v34
	v_ashrrev_i32_e32 v37, 31, v36
	v_or_b32_e32 v38, 0x580, v34
	v_lshl_add_u64 v[36:37], v[36:37], 4, s[0:1]
	v_ashrrev_i32_e32 v39, 31, v38
	v_lshl_add_u64 v[38:39], v[38:39], 4, s[0:1]
	global_load_dwordx4 v[106:109], v[36:37], off
	global_load_dwordx4 v[82:85], v[38:39], off
	v_or_b32_e32 v36, 0x600, v34
	v_ashrrev_i32_e32 v37, 31, v36
	v_or_b32_e32 v38, 0x680, v34
	v_lshl_add_u64 v[36:37], v[36:37], 4, s[0:1]
	v_ashrrev_i32_e32 v39, 31, v38
	v_lshl_add_u64 v[38:39], v[38:39], 4, s[0:1]
	global_load_dwordx4 v[110:113], v[36:37], off
	global_load_dwordx4 v[94:97], v[38:39], off
	v_or_b32_e32 v36, 0x700, v34
	v_ashrrev_i32_e32 v37, 31, v36
	v_or_b32_e32 v34, 0x780, v34
	v_lshl_add_u64 v[36:37], v[36:37], 4, s[0:1]
	v_ashrrev_i32_e32 v35, 31, v34
	v_lshlrev_b32_e32 v23, 3, v199
	s_mulk_i32 s3, 0x840
	v_lshl_add_u64 v[34:35], v[34:35], 4, s[0:1]
	global_load_dwordx4 v[134:137], v[36:37], off
	global_load_dwordx4 v[130:133], v[34:35], off
	v_add_u32_e32 v189, s3, v23
	v_and_b32_e32 v157, 31, v0
	v_lshlrev_b32_e32 v22, 4, v22
	s_movk_i32 s0, 0x210
	v_mad_u32_u24 v179, v157, s0, v22
	s_waitcnt vmcnt(21)
	v_pk_add_f16 v36, v24, v146
	v_pk_add_f16 v37, v25, v147
	s_waitcnt vmcnt(20)
	v_pk_add_f16 v23, v28, v146
	v_pk_mul_f16 v34, v26, v148 clamp
	v_pk_mul_f16 v35, v27, v149 clamp
	v_pk_max_f16 v34, v36, v34
	v_pk_max_f16 v35, v37, v35
	v_pk_add_f16 v38, v29, v147
	v_pk_add_f16 v40, v25, v139
	v_pk_mul_f16 v36, v30, v148 clamp
	v_pk_mul_f16 v37, v31, v149 clamp
	v_pk_max_f16 v36, v23, v36
	v_pk_max_f16 v37, v38, v37
	v_pk_add_f16 v23, v24, v138
	s_nop 0
	v_pk_mul_f16 v38, v26, v140 clamp
	v_pk_mul_f16 v39, v27, v141 clamp
	v_pk_max_f16 v38, v23, v38
	v_pk_max_f16 v39, v40, v39
	v_pk_add_f16 v23, v28, v138
	ds_write2_b64 v189, v[34:35], v[38:39] offset1:66
	v_pk_add_f16 v38, v29, v139
	s_nop 0
	v_pk_mul_f16 v34, v30, v140 clamp
	v_pk_mul_f16 v35, v31, v141 clamp
	v_pk_max_f16 v34, v23, v34
	v_pk_max_f16 v35, v38, v35
	v_add_u32_e32 v23, 0x4000, v189
	ds_write2_b64 v23, v[36:37], v[34:35] offset0:64 offset1:130
	s_waitcnt vmcnt(19)
	v_pk_add_f16 v23, v24, v150
	v_pk_add_f16 v36, v25, v151
	v_pk_add_f16 v38, v29, v151
	v_pk_mul_f16 v34, v26, v152 clamp
	v_pk_mul_f16 v35, v27, v153 clamp
	v_pk_max_f16 v34, v23, v34
	v_pk_max_f16 v35, v36, v35
	v_pk_add_f16 v23, v28, v150
	s_nop 0
	v_pk_mul_f16 v36, v30, v152 clamp
	v_pk_mul_f16 v37, v31, v153 clamp
	v_pk_max_f16 v36, v23, v36
	v_pk_max_f16 v37, v38, v37
	s_waitcnt vmcnt(18)
	v_pk_add_f16 v23, v24, v142
	v_pk_add_f16 v38, v25, v143
	s_nop 0
	v_pk_mul_f16 v24, v26, v144 clamp
	v_pk_mul_f16 v25, v27, v145 clamp
	v_pk_max_f16 v24, v23, v24
	v_pk_max_f16 v25, v38, v25
	v_pk_add_f16 v23, v28, v142
	ds_write2_b64 v189, v[34:35], v[24:25] offset0:132 offset1:198
	v_pk_add_f16 v26, v29, v143
	s_nop 0
	v_pk_mul_f16 v24, v30, v144 clamp
	v_pk_mul_f16 v25, v31, v145 clamp
	v_pk_max_f16 v24, v23, v24
	v_pk_max_f16 v25, v26, v25
	v_add_u32_e32 v23, 0x4400, v189
	v_lshl_add_u64 v[30:31], v[32:33], 0, s[4:5]
	ds_write2_b64 v23, v[36:37], v[24:25] offset0:68 offset1:134
	s_waitcnt lgkmcnt(0)
	s_barrier
	global_load_dwordx4 v[158:161], v[30:31], off
	ds_read_b128 v[22:25], v179
	ds_read_b128 v[26:29], v179 offset:32
	ds_read_b128 v[46:49], v179 offset:64
	ds_read_b128 v[50:53], v179 offset:96
	ds_read_b128 v[54:57], v179 offset:128
	ds_read_b128 v[58:61], v179 offset:160
	v_lshl_add_u64 v[154:155], v[30:31], 0, s[4:5]
	s_waitcnt vmcnt(16) lgkmcnt(5)
	v_mfma_f32_32x32x16_f16 v[30:45], v[122:125], v[22:25], v[2:17]
	ds_read_b128 v[162:165], v179 offset:192
	s_waitcnt vmcnt(15) lgkmcnt(5)
	v_mfma_f32_32x32x16_f16 v[30:45], v[98:101], v[26:29], v[30:45]
	ds_read_b128 v[22:25], v179 offset:224
	s_waitcnt vmcnt(14) lgkmcnt(5)
	v_mfma_f32_32x32x16_f16 v[30:45], v[114:117], v[46:49], v[30:45]
	ds_read_b128 v[26:29], v179 offset:256
	s_waitcnt vmcnt(13) lgkmcnt(5)
	v_mfma_f32_32x32x16_f16 v[30:45], v[86:89], v[50:53], v[30:45]
	ds_read_b128 v[46:49], v179 offset:288
	s_waitcnt vmcnt(12) lgkmcnt(5)
	v_mfma_f32_32x32x16_f16 v[30:45], v[126:129], v[54:57], v[30:45]
	ds_read_b128 v[50:53], v179 offset:320
	s_waitcnt vmcnt(11) lgkmcnt(5)
	v_mfma_f32_32x32x16_f16 v[30:45], v[90:93], v[58:61], v[30:45]
	ds_read_b128 v[54:57], v179 offset:352
	s_waitcnt vmcnt(10) lgkmcnt(5)
	v_mfma_f32_32x32x16_f16 v[30:45], v[118:121], v[162:165], v[30:45]
	ds_read_b128 v[58:61], v179 offset:384
	s_waitcnt vmcnt(9) lgkmcnt(5)
	v_mfma_f32_32x32x16_f16 v[30:45], v[78:81], v[22:25], v[30:45]
	ds_read_b128 v[162:165], v179 offset:416
	s_waitcnt vmcnt(8) lgkmcnt(5)
	v_mfma_f32_32x32x16_f16 v[30:45], v[102:105], v[26:29], v[30:45]
	ds_read_b128 v[22:25], v179 offset:448
	s_waitcnt vmcnt(7) lgkmcnt(5)
	v_mfma_f32_32x32x16_f16 v[30:45], v[74:77], v[46:49], v[30:45]
	ds_read_b128 v[26:29], v179 offset:480
	s_waitcnt vmcnt(6) lgkmcnt(5)
	v_mfma_f32_32x32x16_f16 v[30:45], v[106:109], v[50:53], v[30:45]
	s_waitcnt vmcnt(5) lgkmcnt(4)
	v_mfma_f32_32x32x16_f16 v[30:45], v[82:85], v[54:57], v[30:45]
	s_waitcnt vmcnt(4) lgkmcnt(3)
	v_mfma_f32_32x32x16_f16 v[30:45], v[110:113], v[58:61], v[30:45]
	v_pk_add_f16 v48, v18, v146
	v_pk_add_f16 v49, v19, v147
	s_nop 0
	v_pk_mul_f16 v46, v20, v148 clamp
	v_pk_mul_f16 v47, v21, v149 clamp
	v_pk_max_f16 v46, v48, v46
	v_pk_max_f16 v47, v49, v47
	ds_write_b64 v189, v[46:47] offset:33792
	s_waitcnt vmcnt(3) lgkmcnt(3)
	v_mfma_f32_32x32x16_f16 v[30:45], v[94:97], v[162:165], v[30:45]
	v_pk_add_f16 v48, v18, v138
	v_pk_add_f16 v49, v19, v139
	s_nop 0
	v_pk_mul_f16 v46, v20, v140 clamp
	v_pk_mul_f16 v47, v21, v141 clamp
	v_pk_max_f16 v46, v48, v46
	v_pk_max_f16 v47, v49, v47
	ds_write_b64 v189, v[46:47] offset:34320
	s_waitcnt vmcnt(2) lgkmcnt(3)
	v_mfma_f32_32x32x16_f16 v[30:45], v[134:137], v[22:25], v[30:45]
	v_pk_add_f16 v48, v18, v150
	v_pk_add_f16 v49, v19, v151
	s_nop 0
	v_pk_mul_f16 v46, v20, v152 clamp
	v_pk_mul_f16 v47, v21, v153 clamp
	v_pk_max_f16 v46, v48, v46
	v_pk_max_f16 v47, v49, v47
	ds_write_b64 v189, v[46:47] offset:34848
	s_waitcnt vmcnt(1) lgkmcnt(3)
	v_mfma_f32_32x32x16_f16 v[30:45], v[130:133], v[26:29], v[30:45]
	v_pk_add_f16 v22, v18, v142
	v_pk_add_f16 v23, v19, v143
	s_nop 0
	v_pk_mul_f16 v18, v20, v144 clamp
	v_pk_mul_f16 v19, v21, v145 clamp
	v_pk_max_f16 v18, v22, v18
	v_pk_max_f16 v19, v23, v19
	ds_write_b64 v189, v[18:19] offset:35376
	global_load_dwordx4 v[162:165], v[154:155], off
	ds_read_b128 v[46:49], v179 offset:16896
	ds_read_b128 v[50:53], v179 offset:16928
	ds_read_b128 v[54:57], v179 offset:16960
	ds_read_b128 v[58:61], v179 offset:16992
	ds_read_b128 v[168:171], v179 offset:17024
	ds_read_b128 v[172:175], v179 offset:17056
	s_nop 0
	v_cvt_pk_f16_f32 v167, v30, v31
	v_cvt_pk_f16_f32 v177, v32, v33
	s_waitcnt lgkmcnt(5)
	v_mfma_f32_32x32x16_f16 v[18:33], v[122:125], v[46:49], v[2:17]
	ds_read_b128 v[180:183], v179 offset:17088
	s_waitcnt lgkmcnt(5)
	v_mfma_f32_32x32x16_f16 v[18:33], v[98:101], v[50:53], v[18:33]
	ds_read_b128 v[184:187], v179 offset:17120
	v_exp_f16_e64 v46, v167 clamp
	v_exp_f16_e64 v47, v177 clamp
	v_exp_f16_sdwa v46, v167 clamp dst_sel:WORD_1 dst_unused:UNUSED_PRESERVE src0_sel:WORD_1
	v_exp_f16_sdwa v47, v177 clamp dst_sel:WORD_1 dst_unused:UNUSED_PRESERVE src0_sel:WORD_1
	s_nop 0
	s_waitcnt lgkmcnt(5)
	v_mfma_f32_32x32x16_f16 v[18:33], v[114:117], v[54:57], v[18:33]
	ds_read_b128 v[190:193], v179 offset:17152
	s_movk_i32 s0, 0x3dc5
	v_mov_b32_e32 v178, 0xbdc5
	v_pk_fma_f16 v47, v47, s0, v178 op_sel_hi:[1,0,0]
	v_pk_fma_f16 v46, v46, s0, v178 op_sel_hi:[1,0,0]
	v_pk_max_f16 v47, v177, v47
	v_pk_max_f16 v46, v167, v46
	s_waitcnt lgkmcnt(5)
	v_mfma_f32_32x32x16_f16 v[18:33], v[86:89], v[58:61], v[18:33]
	ds_read_b128 v[194:197], v179 offset:17184
	v_cvt_pk_f16_f32 v48, v34, v35
	v_cvt_pk_f16_f32 v49, v36, v37
	s_waitcnt lgkmcnt(5)
	v_mfma_f32_32x32x16_f16 v[18:33], v[126:129], v[168:171], v[18:33]
	ds_read_b128 v[34:37], v179 offset:17216
	v_exp_f16_e64 v50, v48 clamp
	v_exp_f16_e64 v51, v49 clamp
	v_exp_f16_sdwa v50, v48 clamp dst_sel:WORD_1 dst_unused:UNUSED_PRESERVE src0_sel:WORD_1
	v_exp_f16_sdwa v51, v49 clamp dst_sel:WORD_1 dst_unused:UNUSED_PRESERVE src0_sel:WORD_1
	s_nop 0
	s_waitcnt lgkmcnt(5)
	v_mfma_f32_32x32x16_f16 v[18:33], v[90:93], v[172:175], v[18:33]
	ds_read_b128 v[168:171], v179 offset:17248
	v_pk_fma_f16 v51, v51, s0, v178 op_sel_hi:[1,0,0]
	v_pk_fma_f16 v50, v50, s0, v178 op_sel_hi:[1,0,0]
	v_pk_max_f16 v49, v49, v51
	v_pk_max_f16 v48, v48, v50
	s_waitcnt lgkmcnt(5)
	v_mfma_f32_32x32x16_f16 v[18:33], v[118:121], v[180:183], v[18:33]
	ds_read_b128 v[172:175], v179 offset:17280
	v_cvt_pk_f16_f32 v167, v38, v39
	v_cvt_pk_f16_f32 v177, v40, v41
	v_mfma_f32_16x16x32_f16 v[58:61], v[70:73], v[46:49], 0
	s_waitcnt lgkmcnt(5)
	v_mfma_f32_32x32x16_f16 v[18:33], v[78:81], v[184:187], v[18:33]
	ds_read_b128 v[38:41], v179 offset:17312
	v_exp_f16_e64 v188, v167 clamp
	v_exp_f16_e64 v198, v177 clamp
	v_exp_f16_sdwa v188, v167 clamp dst_sel:WORD_1 dst_unused:UNUSED_PRESERVE src0_sel:WORD_1
	v_exp_f16_sdwa v198, v177 clamp dst_sel:WORD_1 dst_unused:UNUSED_PRESERVE src0_sel:WORD_1
	s_nop 0
	s_waitcnt lgkmcnt(5)
	v_mfma_f32_32x32x16_f16 v[18:33], v[102:105], v[190:193], v[18:33]
	ds_read_b128 v[180:183], v179 offset:17344
	v_pk_fma_f16 v184, v198, s0, v178 op_sel_hi:[1,0,0]
	s_nop 0
	v_pk_max_f16 v185, v177, v184
	v_pk_fma_f16 v177, v188, s0, v178 op_sel_hi:[1,0,0]
	s_nop 0
	v_pk_max_f16 v184, v167, v177
	s_waitcnt lgkmcnt(5)
	v_mfma_f32_32x32x16_f16 v[18:33], v[74:77], v[194:197], v[18:33]
	ds_read_b128 v[190:193], v179 offset:17376
	v_cvt_pk_f16_f32 v42, v42, v43
	v_cvt_pk_f16_f32 v43, v44, v45
	s_waitcnt lgkmcnt(5)
	v_mfma_f32_32x32x16_f16 v[18:33], v[106:109], v[34:37], v[18:33]
	v_exp_f16_e64 v44, v42 clamp
	v_exp_f16_e64 v45, v43 clamp
	v_exp_f16_sdwa v44, v42 clamp dst_sel:WORD_1 dst_unused:UNUSED_PRESERVE src0_sel:WORD_1
	v_exp_f16_sdwa v45, v43 clamp dst_sel:WORD_1 dst_unused:UNUSED_PRESERVE src0_sel:WORD_1
	s_nop 0
	s_waitcnt lgkmcnt(4)
	v_mfma_f32_32x32x16_f16 v[18:33], v[82:85], v[168:171], v[18:33]
	v_pk_fma_f16 v34, v45, s0, v178 op_sel_hi:[1,0,0]
	s_nop 0
	v_pk_max_f16 v187, v43, v34
	v_pk_fma_f16 v34, v44, s0, v178 op_sel_hi:[1,0,0]
	s_nop 0
	v_pk_max_f16 v186, v42, v34
	s_waitcnt lgkmcnt(3)
	v_mfma_f32_32x32x16_f16 v[18:33], v[110:113], v[172:175], v[18:33]
	v_pk_add_f16 v36, v62, v146
	v_pk_add_f16 v37, v63, v147
	s_nop 0
	v_pk_mul_f16 v34, v64, v148 clamp
	v_pk_mul_f16 v35, v65, v149 clamp
	v_pk_max_f16 v34, v36, v34
	v_pk_max_f16 v35, v37, v35
	ds_write_b64 v189, v[34:35] offset:50688
	v_mfma_f32_16x16x32_f16 v[58:61], v[66:69], v[184:187], v[58:61]
	s_waitcnt lgkmcnt(3)
	v_mfma_f32_32x32x16_f16 v[18:33], v[94:97], v[38:41], v[18:33]
	v_pk_add_f16 v36, v62, v138
	v_pk_add_f16 v37, v63, v139
	s_nop 0
	v_pk_mul_f16 v34, v64, v140 clamp
	v_pk_mul_f16 v35, v65, v141 clamp
	v_pk_max_f16 v34, v36, v34
	v_pk_max_f16 v35, v37, v35
	ds_write_b64 v189, v[34:35] offset:51216
	s_waitcnt lgkmcnt(3)
	v_mfma_f32_32x32x16_f16 v[18:33], v[134:137], v[180:183], v[18:33]
	v_pk_add_f16 v36, v62, v150
	v_pk_add_f16 v37, v63, v151
	s_nop 0
	v_pk_mul_f16 v34, v64, v152 clamp
	v_pk_mul_f16 v35, v65, v153 clamp
	v_pk_max_f16 v34, v36, v34
	v_pk_max_f16 v35, v37, v35
	ds_write_b64 v189, v[34:35] offset:51744
	s_waitcnt lgkmcnt(3)
	v_mfma_f32_32x32x16_f16 v[18:33], v[130:133], v[190:193], v[18:33]
	v_pk_add_f16 v36, v62, v142
	v_pk_add_f16 v37, v63, v143
	s_nop 0
	v_pk_mul_f16 v34, v64, v144 clamp
	v_pk_mul_f16 v35, v65, v145 clamp
	v_pk_max_f16 v34, v36, v34
	v_pk_max_f16 v35, v37, v35
	ds_write_b64 v189, v[34:35] offset:52272
	v_and_b32_e32 v157, 15, v199
	v_lshrrev_b32_e32 v1, 5, v199
	v_lshl_or_b32 v157, v1, 4, v157
	v_bfe_u32 v1, v199, 4, 1
	v_lshlrev_b32_e32 v1, 2, v1
	v_or_b32_e32 v178, s2, v157
	v_mul_lo_u32 v167, v178, 7
	v_add_u32_e32 v170, v167, v1
	v_mov_b32_e32 v34, 0x10800
	v_lshl_add_u32 v206, v170, 2, v34
	v_and_b32_e32 v34, 16, v199
	v_cmp_eq_u32_e64 s[0:1], 0, v34
	v_mov_b32_e32 v34, 0x10808
	v_lshl_add_u32 v34, v167, 2, v34
	v_or_b32_e32 v36, 3, v1
	v_mul_i32_i24_e32 v34, -6, v156
	v_mul_u32_u24_e32 v35, 7, v156
	v_cmp_gt_u32_e64 s[2:3], 6, v36
	v_lshlrev_b32_e32 v171, 2, v167
	v_lshlrev_b32_e32 v172, 2, v36
	s_mov_b32 s5, 0x10800
	v_add3_u32 v36, v171, v172, s5
	ds_write2_b32 v206, v58, v59 offset1:1
	s_and_saveexec_b64 s[2:3], s[0:1]
	ds_write2_b32 v206, v60, v61 offset0:2 offset1:3
	s_or_b64 exec, exec, s[2:3]
	s_sub_i32 s9, 0xff, s28
	s_mul_i32 s9, s9, s28
	s_not_b32 s25, s28
	s_ashr_i32 s9, s9, 1
	s_add_i32 s24, s24, s25
	s_add_i32 s24, s24, s9
	s_mul_i32 s8, s39, 0x1fc0
	s_ashr_i32 s9, s24, 31
	s_mul_hi_u32 s5, s39, 0x1fc0
	s_add_u32 s8, s8, s24
	s_addc_u32 s5, s5, s9
	s_mul_i32 s5, s5, 6
	s_mul_hi_u32 s9, s8, 6
	s_add_i32 s9, s9, s5
	v_add_u32_e32 v34, v34, v0
	s_cmpk_lt_u32 s21, 0xc0
	v_add_u32_e32 v173, v34, v35
	v_lshl_or_b32 v177, v34, 8, v156
	s_mul_i32 s8, s8, 6
	s_cselect_b64 s[24:25], -1, 0
	s_cmpk_gt_u32 s21, 0xbf
	s_waitcnt lgkmcnt(0)
	s_barrier
	s_cbranch_scc1 .LBB1_33
	s_andn2_b64 vcc, exec, s[6:7]
	s_mov_b64 s[6:7], -1
	s_cbranch_vccnz .LBB1_29
	s_movk_i32 s5, 0x60
	v_cmp_gt_u32_e32 vcc, s5, v0
	s_and_saveexec_b64 s[6:7], vcc
	s_cbranch_execz .LBB1_28
	v_lshlrev_b32_e32 v38, 2, v173
	v_add_u32_e32 v46, 0x10800, v38
	ds_read2_b32 v[34:35], v46 offset1:224
	v_add_u32_e32 v36, 0x700, v46
	ds_read2_b32 v[36:37], v36 offset1:224
	v_add_u32_e32 v39, 0x109c0, v38
	v_add_u32_e32 v40, 0x10d40, v38
	v_add_u32_e32 v41, 0x110c0, v38
	v_add_u32_e32 v42, 0x11440, v38
	v_add_u32_e32 v43, 0x117c0, v38
	v_add_u32_e32 v44, 0x11b40, v38
	v_add_u32_e32 v45, 0x11ec0, v38
	v_add_u32_e32 v47, 0x12240, v38
	ds_read_b32 v38, v39
	ds_read_b32 v39, v40
	ds_read_b32 v40, v41
	ds_read_b32 v41, v42
	ds_read_b32 v42, v43
	ds_read_b32 v43, v44
	ds_read_b32 v44, v45
	ds_read_b32 v45, v47
	s_waitcnt lgkmcnt(6)
	v_pk_add_f32 v[34:35], v[34:35], v[38:39]
	s_lshl_b64 s[26:27], s[8:9], 2
	v_add_f32_e32 v34, 0, v34
	v_add_f32_e32 v38, v34, v35
	s_waitcnt lgkmcnt(4)
	v_pk_add_f32 v[34:35], v[36:37], v[40:41]
	v_add_u32_e32 v36, 0xe00, v46
	ds_read2_b32 v[36:37], v36 offset1:224
	v_add_f32_e32 v34, v38, v34
	v_add_u32_e32 v38, 0x1500, v46
	ds_read2_b32 v[38:39], v38 offset1:224
	v_add_f32_e32 v40, v34, v35
	s_waitcnt lgkmcnt(1)
	v_pk_add_f32 v[34:35], v[36:37], v[42:43]
	s_add_u32 s26, s10, s26
	v_add_f32_e32 v34, v40, v34
	v_add_f32_e32 v36, v34, v35
	s_waitcnt lgkmcnt(0)
	v_pk_add_f32 v[34:35], v[38:39], v[44:45]
	s_addc_u32 s27, s11, s27
	v_add_f32_e32 v34, v36, v34
	v_add_f32_e32 v34, v34, v35
	v_fmamk_f32 v34, v34, 0x3eb17218, v176
	v_lshlrev_b32 v35, 2, v0
	global_store_dword v35, v34, s[26:27]

.LBB1_33:
	s_mov_b32 s5, 0
	v_lshl_add_u64 v[168:169], v[154:155], 0, s[4:5]
	global_load_dwordx4 v[154:157], v[168:169], off
	ds_read_b128 v[50:53], v179 offset:33792
	ds_read_b128 v[54:57], v179 offset:33824
	ds_read_b128 v[58:61], v179 offset:33856
	ds_read_b128 v[62:65], v179 offset:33888
	ds_read_b128 v[180:183], v179 offset:33920
	ds_read_b128 v[184:187], v179 offset:33952
	s_waitcnt lgkmcnt(5)
	v_mfma_f32_32x32x16_f16 v[34:49], v[122:125], v[50:53], v[2:17]
	ds_read_b128 v[190:193], v179 offset:33984
	v_cvt_pk_f16_f32 v174, v18, v19
	v_cvt_pk_f16_f32 v175, v20, v21
	s_waitcnt lgkmcnt(5)
	v_mfma_f32_32x32x16_f16 v[34:49], v[98:101], v[54:57], v[34:49]
	ds_read_b128 v[18:21], v179 offset:34016
	v_exp_f16_e64 v50, v174 clamp
	v_exp_f16_e64 v51, v175 clamp
	v_exp_f16_sdwa v50, v174 clamp dst_sel:WORD_1 dst_unused:UNUSED_PRESERVE src0_sel:WORD_1
	v_exp_f16_sdwa v51, v175 clamp dst_sel:WORD_1 dst_unused:UNUSED_PRESERVE src0_sel:WORD_1
	s_nop 0
	s_waitcnt lgkmcnt(5)
	v_mfma_f32_32x32x16_f16 v[34:49], v[114:117], v[58:61], v[34:49]
	ds_read_b128 v[194:197], v179 offset:34048
	s_movk_i32 s5, 0x3dc5
	v_mov_b32_e32 v188, 0xbdc5
	v_pk_fma_f16 v51, v51, s5, v188 op_sel_hi:[1,0,0]
	v_pk_fma_f16 v50, v50, s5, v188 op_sel_hi:[1,0,0]
	v_pk_max_f16 v51, v175, v51
	v_pk_max_f16 v50, v174, v50
	s_waitcnt lgkmcnt(5)
	v_mfma_f32_32x32x16_f16 v[34:49], v[86:89], v[62:65], v[34:49]
	ds_read_b128 v[200:203], v179 offset:34080
	v_cvt_pk_f16_f32 v52, v22, v23
	v_cvt_pk_f16_f32 v53, v24, v25
	s_waitcnt lgkmcnt(5)
	v_mfma_f32_32x32x16_f16 v[34:49], v[126:129], v[180:183], v[34:49]
	ds_read_b128 v[22:25], v179 offset:34112
	v_exp_f16_e64 v54, v52 clamp
	v_exp_f16_e64 v55, v53 clamp
	v_exp_f16_sdwa v54, v52 clamp dst_sel:WORD_1 dst_unused:UNUSED_PRESERVE src0_sel:WORD_1
	v_exp_f16_sdwa v55, v53 clamp dst_sel:WORD_1 dst_unused:UNUSED_PRESERVE src0_sel:WORD_1
	s_nop 0
	s_waitcnt lgkmcnt(5)
	v_mfma_f32_32x32x16_f16 v[34:49], v[90:93], v[184:187], v[34:49]
	ds_read_b128 v[180:183], v179 offset:34144
	v_pk_fma_f16 v55, v55, s5, v188 op_sel_hi:[1,0,0]
	v_pk_fma_f16 v54, v54, s5, v188 op_sel_hi:[1,0,0]
	v_pk_max_f16 v53, v53, v55
	v_pk_max_f16 v52, v52, v54
	s_waitcnt lgkmcnt(5)
	v_mfma_f32_32x32x16_f16 v[34:49], v[118:121], v[190:193], v[34:49]
	ds_read_b128 v[184:187], v179 offset:34176
	v_cvt_pk_f16_f32 v174, v26, v27
	v_cvt_pk_f16_f32 v175, v28, v29
	v_mfma_f32_16x16x32_f16 v[62:65], v[70:73], v[50:53], 0
	s_waitcnt lgkmcnt(5)
	v_mfma_f32_32x32x16_f16 v[34:49], v[78:81], v[18:21], v[34:49]
	ds_read_b128 v[26:29], v179 offset:34208
	v_exp_f16_e64 v190, v174 clamp
	v_exp_f16_e64 v191, v175 clamp
	v_exp_f16_sdwa v190, v174 clamp dst_sel:WORD_1 dst_unused:UNUSED_PRESERVE src0_sel:WORD_1
	v_exp_f16_sdwa v191, v175 clamp dst_sel:WORD_1 dst_unused:UNUSED_PRESERVE src0_sel:WORD_1
	s_nop 0
	s_waitcnt lgkmcnt(5)
	v_mfma_f32_32x32x16_f16 v[34:49], v[102:105], v[194:197], v[34:49]
	ds_read_b128 v[18:21], v179 offset:34240
	v_pk_fma_f16 v191, v191, s5, v188 op_sel_hi:[1,0,0]
	s_nop 0
	v_pk_max_f16 v191, v175, v191
	v_pk_fma_f16 v175, v190, s5, v188 op_sel_hi:[1,0,0]
	s_nop 0
	v_pk_max_f16 v190, v174, v175
	s_waitcnt lgkmcnt(5)
	v_mfma_f32_32x32x16_f16 v[34:49], v[74:77], v[200:203], v[34:49]
	ds_read_b128 v[194:197], v179 offset:34272
	v_cvt_pk_f16_f32 v30, v30, v31
	v_cvt_pk_f16_f32 v31, v32, v33
	s_waitcnt lgkmcnt(5)
	v_mfma_f32_32x32x16_f16 v[34:49], v[106:109], v[22:25], v[34:49]
	v_exp_f16_e64 v32, v30 clamp
	v_exp_f16_e64 v33, v31 clamp
	v_exp_f16_sdwa v32, v30 clamp dst_sel:WORD_1 dst_unused:UNUSED_PRESERVE src0_sel:WORD_1
	v_exp_f16_sdwa v33, v31 clamp dst_sel:WORD_1 dst_unused:UNUSED_PRESERVE src0_sel:WORD_1
	s_nop 0
	s_waitcnt lgkmcnt(4)
	v_mfma_f32_32x32x16_f16 v[34:49], v[82:85], v[180:183], v[34:49]
	v_pk_fma_f16 v22, v33, s5, v188 op_sel_hi:[1,0,0]
	s_nop 0
	v_pk_max_f16 v193, v31, v22
	v_pk_fma_f16 v22, v32, s5, v188 op_sel_hi:[1,0,0]
	s_nop 0
	v_pk_max_f16 v192, v30, v22
	s_waitcnt lgkmcnt(3)
	v_mfma_f32_32x32x16_f16 v[34:49], v[110:113], v[184:187], v[34:49]
	s_waitcnt vmcnt(2)
	v_pk_add_f16 v24, v158, v146
	v_pk_add_f16 v25, v159, v147
	s_nop 0
	v_pk_mul_f16 v22, v160, v148 clamp
	v_pk_mul_f16 v23, v161, v149 clamp
	v_pk_max_f16 v22, v24, v22
	v_pk_max_f16 v23, v25, v23
	ds_write_b64 v189, v[22:23]
	v_mfma_f32_16x16x32_f16 v[62:65], v[66:69], v[190:193], v[62:65]
	s_waitcnt lgkmcnt(3)
	v_mfma_f32_32x32x16_f16 v[34:49], v[94:97], v[26:29], v[34:49]
	v_pk_add_f16 v24, v158, v138
	v_pk_add_f16 v25, v159, v139
	s_nop 0
	v_pk_mul_f16 v22, v160, v140 clamp
	v_pk_mul_f16 v23, v161, v141 clamp
	v_pk_max_f16 v22, v24, v22
	v_pk_max_f16 v23, v25, v23
	ds_write_b64 v189, v[22:23] offset:528
	s_waitcnt lgkmcnt(3)
	v_mfma_f32_32x32x16_f16 v[34:49], v[134:137], v[18:21], v[34:49]
	v_pk_add_f16 v24, v158, v150
	v_pk_add_f16 v25, v159, v151
	s_nop 0
	v_pk_mul_f16 v22, v160, v152 clamp
	v_pk_mul_f16 v23, v161, v153 clamp
	v_pk_max_f16 v22, v24, v22
	v_pk_max_f16 v23, v25, v23
	ds_write_b64 v189, v[22:23] offset:1056
	s_waitcnt lgkmcnt(3)
	v_mfma_f32_32x32x16_f16 v[34:49], v[130:133], v[194:197], v[34:49]
	v_pk_add_f16 v20, v158, v142
	v_pk_add_f16 v21, v159, v143
	s_nop 0
	v_pk_mul_f16 v18, v160, v144 clamp
	v_pk_mul_f16 v19, v161, v145 clamp
	v_pk_max_f16 v18, v20, v18
	v_pk_max_f16 v19, v21, v19
	ds_write_b64 v189, v[18:19] offset:1584
	v_mov_b32_e32 v18, 0x12400
	v_lshl_add_u32 v201, v170, 2, v18
	v_mov_b32_e32 v18, 0x12408
	v_lshl_add_u32 v18, v167, 2, v18
	s_mov_b32 s5, 0x12400
	v_add3_u32 v18, v171, v172, s5
	ds_write2_b32 v201, v62, v63 offset1:1
	s_and_saveexec_b64 s[6:7], s[0:1]
	ds_write2_b32 v201, v64, v65 offset0:2 offset1:3
	s_or_b64 exec, exec, s[6:7]
	s_mov_b32 s5, 0
	v_lshl_add_u64 v[168:169], v[168:169], 0, s[4:5]
	global_load_dwordx4 v[158:161], v[168:169], off
	ds_read_b128 v[50:53], v179 offset:50688
	ds_read_b128 v[54:57], v179 offset:50720
	ds_read_b128 v[58:61], v179 offset:50752
	ds_read_b128 v[62:65], v179 offset:50784
	ds_read_b128 v[180:183], v179 offset:50816
	ds_read_b128 v[184:187], v179 offset:50848
	s_waitcnt lgkmcnt(5)
	v_mfma_f32_32x32x16_f16 v[18:33], v[122:125], v[50:53], v[2:17]
	ds_read_b128 v[190:193], v179 offset:50880
	v_cvt_pk_f16_f32 v174, v34, v35
	v_cvt_pk_f16_f32 v175, v36, v37
	s_waitcnt lgkmcnt(5)
	v_mfma_f32_32x32x16_f16 v[18:33], v[98:101], v[54:57], v[18:33]
	ds_read_b128 v[34:37], v179 offset:50912
	v_exp_f16_e64 v50, v174 clamp
	v_exp_f16_e64 v51, v175 clamp
	v_exp_f16_sdwa v50, v174 clamp dst_sel:WORD_1 dst_unused:UNUSED_PRESERVE src0_sel:WORD_1
	v_exp_f16_sdwa v51, v175 clamp dst_sel:WORD_1 dst_unused:UNUSED_PRESERVE src0_sel:WORD_1
	s_nop 0
	s_waitcnt lgkmcnt(5)
	v_mfma_f32_32x32x16_f16 v[18:33], v[114:117], v[58:61], v[18:33]
	ds_read_b128 v[194:197], v179 offset:50944
	s_movk_i32 s5, 0x3dc5
	v_mov_b32_e32 v188, 0xbdc5
	v_pk_fma_f16 v51, v51, s5, v188 op_sel_hi:[1,0,0]
	v_pk_fma_f16 v50, v50, s5, v188 op_sel_hi:[1,0,0]
	v_pk_max_f16 v51, v175, v51
	v_pk_max_f16 v50, v174, v50
	s_waitcnt lgkmcnt(5)
	v_mfma_f32_32x32x16_f16 v[18:33], v[86:89], v[62:65], v[18:33]
	ds_read_b128 v[202:205], v179 offset:50976
	v_cvt_pk_f16_f32 v52, v38, v39
	v_cvt_pk_f16_f32 v53, v40, v41
	s_waitcnt lgkmcnt(5)
	v_mfma_f32_32x32x16_f16 v[18:33], v[126:129], v[180:183], v[18:33]
	ds_read_b128 v[38:41], v179 offset:51008
	v_exp_f16_e64 v54, v52 clamp
	v_exp_f16_e64 v55, v53 clamp
	v_exp_f16_sdwa v54, v52 clamp dst_sel:WORD_1 dst_unused:UNUSED_PRESERVE src0_sel:WORD_1
	v_exp_f16_sdwa v55, v53 clamp dst_sel:WORD_1 dst_unused:UNUSED_PRESERVE src0_sel:WORD_1
	s_nop 0
	s_waitcnt lgkmcnt(5)
	v_mfma_f32_32x32x16_f16 v[18:33], v[90:93], v[184:187], v[18:33]
	ds_read_b128 v[180:183], v179 offset:51040
	v_pk_fma_f16 v55, v55, s5, v188 op_sel_hi:[1,0,0]
	v_pk_fma_f16 v54, v54, s5, v188 op_sel_hi:[1,0,0]
	v_pk_max_f16 v53, v53, v55
	v_pk_max_f16 v52, v52, v54
	s_waitcnt lgkmcnt(5)
	v_mfma_f32_32x32x16_f16 v[18:33], v[118:121], v[190:193], v[18:33]
	ds_read_b128 v[184:187], v179 offset:51072
	v_cvt_pk_f16_f32 v174, v42, v43
	v_cvt_pk_f16_f32 v175, v44, v45
	v_mfma_f32_16x16x32_f16 v[62:65], v[70:73], v[50:53], 0
	s_waitcnt lgkmcnt(5)
	v_mfma_f32_32x32x16_f16 v[18:33], v[78:81], v[34:37], v[18:33]
	ds_read_b128 v[42:45], v179 offset:51104
	v_exp_f16_e64 v190, v174 clamp
	v_exp_f16_e64 v191, v175 clamp
	v_exp_f16_sdwa v190, v174 clamp dst_sel:WORD_1 dst_unused:UNUSED_PRESERVE src0_sel:WORD_1
	v_exp_f16_sdwa v191, v175 clamp dst_sel:WORD_1 dst_unused:UNUSED_PRESERVE src0_sel:WORD_1
	s_nop 0
	s_waitcnt lgkmcnt(5)
	v_mfma_f32_32x32x16_f16 v[18:33], v[102:105], v[194:197], v[18:33]
	ds_read_b128 v[34:37], v179 offset:51136
	v_pk_fma_f16 v191, v191, s5, v188 op_sel_hi:[1,0,0]
	s_nop 0
	v_pk_max_f16 v191, v175, v191
	v_pk_fma_f16 v175, v190, s5, v188 op_sel_hi:[1,0,0]
	s_nop 0
	v_pk_max_f16 v190, v174, v175
	s_waitcnt lgkmcnt(5)
	v_mfma_f32_32x32x16_f16 v[18:33], v[74:77], v[202:205], v[18:33]
	ds_read_b128 v[194:197], v179 offset:51168
	v_cvt_pk_f16_f32 v46, v46, v47
	v_cvt_pk_f16_f32 v47, v48, v49
	s_waitcnt lgkmcnt(5)
	v_mfma_f32_32x32x16_f16 v[18:33], v[106:109], v[38:41], v[18:33]
	v_exp_f16_e64 v48, v46 clamp
	v_exp_f16_e64 v49, v47 clamp
	v_exp_f16_sdwa v48, v46 clamp dst_sel:WORD_1 dst_unused:UNUSED_PRESERVE src0_sel:WORD_1
	v_exp_f16_sdwa v49, v47 clamp dst_sel:WORD_1 dst_unused:UNUSED_PRESERVE src0_sel:WORD_1
	s_nop 0
	s_waitcnt lgkmcnt(4)
	v_mfma_f32_32x32x16_f16 v[18:33], v[82:85], v[180:183], v[18:33]
	v_pk_fma_f16 v38, v49, s5, v188 op_sel_hi:[1,0,0]
	s_nop 0
	v_pk_max_f16 v193, v47, v38
	v_pk_fma_f16 v38, v48, s5, v188 op_sel_hi:[1,0,0]
	s_nop 0
	v_pk_max_f16 v192, v46, v38
	s_waitcnt lgkmcnt(3)
	v_mfma_f32_32x32x16_f16 v[18:33], v[110:113], v[184:187], v[18:33]
	s_waitcnt vmcnt(2)
	v_pk_add_f16 v40, v162, v146
	v_pk_add_f16 v41, v163, v147
	s_nop 0
	v_pk_mul_f16 v38, v164, v148 clamp
	v_pk_mul_f16 v39, v165, v149 clamp
	v_pk_max_f16 v38, v40, v38
	v_pk_max_f16 v39, v41, v39
	ds_write_b64 v189, v[38:39] offset:16896
	v_mfma_f32_16x16x32_f16 v[62:65], v[66:69], v[190:193], v[62:65]
	s_waitcnt lgkmcnt(3)
	v_mfma_f32_32x32x16_f16 v[18:33], v[94:97], v[42:45], v[18:33]
	v_pk_add_f16 v40, v162, v138
	v_pk_add_f16 v41, v163, v139
	s_nop 0
	v_pk_mul_f16 v38, v164, v140 clamp
	v_pk_mul_f16 v39, v165, v141 clamp
	v_pk_max_f16 v38, v40, v38
	v_pk_max_f16 v39, v41, v39
	ds_write_b64 v189, v[38:39] offset:17424
	s_waitcnt lgkmcnt(3)
	v_mfma_f32_32x32x16_f16 v[18:33], v[134:137], v[34:37], v[18:33]
	v_pk_add_f16 v40, v162, v150
	v_pk_add_f16 v41, v163, v151
	s_nop 0
	v_pk_mul_f16 v38, v164, v152 clamp
	v_pk_mul_f16 v39, v165, v153 clamp
	v_pk_max_f16 v38, v40, v38
	v_pk_max_f16 v39, v41, v39
	ds_write_b64 v189, v[38:39] offset:17952
	s_waitcnt lgkmcnt(3)
	v_mfma_f32_32x32x16_f16 v[18:33], v[130:133], v[194:197], v[18:33]
	v_pk_add_f16 v36, v162, v142
	v_pk_add_f16 v37, v163, v143
	s_nop 0
	v_pk_mul_f16 v34, v164, v144 clamp
	v_pk_mul_f16 v35, v165, v145 clamp
	v_pk_max_f16 v34, v36, v34
	v_pk_max_f16 v35, v37, v35
	ds_write_b64 v189, v[34:35] offset:18480
	v_mov_b32_e32 v34, 0x14000
	v_lshl_add_u32 v211, v170, 2, v34
	v_mov_b32_e32 v34, 0x14008
	v_lshl_add_u32 v34, v167, 2, v34
	s_mov_b32 s5, 0x14000
	v_add3_u32 v34, v171, v172, s5
	ds_write2_b32 v211, v62, v63 offset1:1
	s_and_saveexec_b64 s[6:7], s[0:1]
	ds_write2_b32 v211, v64, v65 offset0:2 offset1:3
	s_or_b64 exec, exec, s[6:7]
	s_mov_b32 s21, 0
	s_mov_b32 s5, s21
	v_lshl_add_u64 v[168:169], v[168:169], 0, s[4:5]
	s_sub_i32 s4, 0x7e, s28
	s_mul_i32 s4, s4, 6
	s_ashr_i32 s5, s4, 31
	s_add_u32 s26, s8, s4
	s_addc_u32 s27, s9, s5
	s_or_b32 s31, s28, 1
	s_or_b64 s[4:5], s[18:19], s[22:23]
	s_and_b64 s[4:5], s[4:5], exec
	s_cselect_b32 s6, s13, s46
	s_cselect_b32 s7, s12, s45
	s_lshl_b32 s4, s30, 6
	s_ashr_i32 s5, s4, 31
	s_lshl_b64 s[4:5], s[4:5], 4
	s_add_u32 s4, s7, s4
	s_addc_u32 s5, s6, s5
	s_lshl_b32 s51, s29, 4
	s_sub_i32 s9, 0xff, s51
	s_mul_i32 s9, s9, s51
	s_sub_i32 s28, s43, s29
	s_ashr_i32 s9, s9, 1
	s_lshl_b32 s28, s28, 4
	s_add_i32 s9, s28, s9
	s_add_i32 s9, s9, -1
	s_mul_i32 s8, s33, 0x1fc0
	s_ashr_i32 s28, s9, 31
	v_mov_b32_e32 v167, 0
	v_lshlrev_b32_e32 v34, 2, v173
	s_add_u32 s8, s9, s8
	v_lshl_add_u64 v[174:175], s[4:5], 0, v[166:167]
	v_cndmask_b32_e64 v231, 0, 1, s[16:17]
	s_movk_i32 s4, 0xc0
	v_add_u32_e32 v200, 0x12400, v34
	s_addc_u32 s9, s28, 0
	v_add_u32_e32 v190, 0x14000, v34
	v_add_u32_e32 v180, 0x15c00, v34
	v_add_u32_e32 v216, 0x10800, v34
	v_add_u32_e32 v209, 0x125c0, v34
	v_add_u32_e32 v210, 0x12940, v34
	v_add_u32_e32 v207, 0x12cc0, v34
	v_add_u32_e32 v208, 0x13040, v34
	v_add_u32_e32 v204, 0x133c0, v34
	v_add_u32_e32 v205, 0x13740, v34
	v_add_u32_e32 v202, 0x13ac0, v34
	v_add_u32_e32 v203, 0x13e40, v34
	v_add_u32_e32 v197, 0x141c0, v34
	v_add_u32_e32 v198, 0x14540, v34
	v_add_u32_e32 v195, 0x148c0, v34
	v_add_u32_e32 v196, 0x14c40, v34
	v_add_u32_e32 v193, 0x14fc0, v34
	v_add_u32_e32 v194, 0x15340, v34
	v_add_u32_e32 v191, 0x156c0, v34
	v_add_u32_e32 v192, 0x15a40, v34
	v_add_u32_e32 v187, 0x15dc0, v34
	v_add_u32_e32 v188, 0x16140, v34
	v_add_u32_e32 v185, 0x164c0, v34
	v_add_u32_e32 v186, 0x16840, v34
	v_add_u32_e32 v183, 0x16bc0, v34
	v_add_u32_e32 v184, 0x16f40, v34
	v_add_u32_e32 v181, 0x172c0, v34
	v_add_u32_e32 v182, 0x17640, v34
	v_add_u32_e32 v223, 0x109c0, v34
	v_add_u32_e32 v224, 0x10d40, v34
	v_add_u32_e32 v221, 0x110c0, v34
	v_add_u32_e32 v222, 0x11440, v34
	v_add_u32_e32 v219, 0x117c0, v34
	v_add_u32_e32 v220, 0x11b40, v34
	v_add_u32_e32 v217, 0x11ec0, v34
	v_add_u32_e32 v218, 0x12240, v34
	v_mov_b32_e32 v34, 0x17800
	v_cndmask_b32_e64 v230, 0, 1, s[18:19]
	v_readfirstlane_b32 s50, v231
	v_cmp_gt_u32_e64 s[6:7], s4, v0
	s_movk_i32 s4, 0x60
	s_mul_i32 s9, s9, 6
	s_mul_hi_u32 s28, s8, 6
	v_mov_b32_e32 v35, 0x15c00
	v_add_u32_e32 v228, 0x15c00, v171
	v_add_u32_e32 v226, 0x10800, v171
	v_add_u32_e32 v215, 0x12400, v171
	v_add_u32_e32 v213, 0x14000, v171
	v_lshl_add_u32 v232, v177, 2, v34
	v_cndmask_b32_e64 v34, 0, 1, s[24:25]
	s_mov_b32 s48, 1
	v_readfirstlane_b32 s49, v230
	v_cmp_gt_u32_e64 s[4:5], s4, v0
	s_add_i32 s52, s28, s9
	s_mul_i32 s53, s8, 6
	v_lshl_add_u32 v229, v170, 2, v35
	v_add_u32_e32 v227, v228, v172
	v_add_u32_e32 v225, v226, v172
	v_add_u32_e32 v214, v215, v172
	v_add_u32_e32 v212, v213, v172
	s_mov_b32 s56, 8
	s_mov_b32 s54, 16
	v_cmp_ne_u32_e64 s[8:9], 1, v34
	s_movk_i32 s55, 0x3dc5
	v_mov_b32_e32 v233, 0xbdc5
	v_add_u32_e32 v234, 0x700, v200
	v_add_u32_e32 v235, 0xe00, v200
	v_add_u32_e32 v236, 0x1500, v200
	v_add_u32_e32 v237, 0x700, v190
	v_add_u32_e32 v238, 0xe00, v190
	v_add_u32_e32 v239, 0x1500, v190
	s_mov_b32 s41, s50
	s_waitcnt lgkmcnt(0)
	s_barrier
	ds_read_b128 v[50:53], v179
	ds_read_b128 v[54:57], v179 offset:32
	ds_read_b128 v[58:61], v179 offset:64
	ds_read_b128 v[62:65], v179 offset:96
	ds_read_b128 v[170:173], v179 offset:128
	ds_read_b128 v[240:243], v179 offset:160
	s_and_b64 vcc, exec, s[8:9]
	s_cbranch_vccnz .LBB1_50

.LBB1_59:
	global_load_dwordx4 v[162:165], v[168:169], off
	s_waitcnt lgkmcnt(5)
	v_mfma_f32_32x32x16_f16 v[34:49], v[122:125], v[50:53], v[2:17]
	ds_read_b128 v[244:247], v179 offset:192
	v_cvt_pk_f16_f32 v166, v18, v19
	v_cvt_pk_f16_f32 v167, v20, v21
	s_waitcnt lgkmcnt(5)
	v_mfma_f32_32x32x16_f16 v[34:49], v[98:101], v[54:57], v[34:49]
	ds_read_b128 v[18:21], v179 offset:224
	v_exp_f16_e64 v50, v166 clamp
	v_exp_f16_e64 v51, v167 clamp
	v_exp_f16_sdwa v50, v166 clamp dst_sel:WORD_1 dst_unused:UNUSED_PRESERVE src0_sel:WORD_1
	v_exp_f16_sdwa v51, v167 clamp dst_sel:WORD_1 dst_unused:UNUSED_PRESERVE src0_sel:WORD_1
	s_nop 0
	s_waitcnt lgkmcnt(5)
	v_mfma_f32_32x32x16_f16 v[34:49], v[114:117], v[58:61], v[34:49]
	ds_read_b128 v[248:251], v179 offset:256
	v_pk_fma_f16 v51, v51, s55, v233 op_sel_hi:[1,0,0]
	v_pk_fma_f16 v50, v50, s55, v233 op_sel_hi:[1,0,0]
	v_pk_max_f16 v51, v167, v51
	v_pk_max_f16 v50, v166, v50
	s_waitcnt lgkmcnt(5)
	v_mfma_f32_32x32x16_f16 v[34:49], v[86:89], v[62:65], v[34:49]
	ds_read_b128 v[252:255], v179 offset:288
	v_cvt_pk_f16_f32 v52, v22, v23
	v_cvt_pk_f16_f32 v53, v24, v25
	s_waitcnt lgkmcnt(5)
	v_mfma_f32_32x32x16_f16 v[34:49], v[126:129], v[170:173], v[34:49]
	ds_read_b128 v[22:25], v179 offset:320
	v_exp_f16_e64 v54, v52 clamp
	v_exp_f16_e64 v55, v53 clamp
	v_exp_f16_sdwa v54, v52 clamp dst_sel:WORD_1 dst_unused:UNUSED_PRESERVE src0_sel:WORD_1
	v_exp_f16_sdwa v55, v53 clamp dst_sel:WORD_1 dst_unused:UNUSED_PRESERVE src0_sel:WORD_1
	s_nop 0
	s_waitcnt lgkmcnt(5)
	v_mfma_f32_32x32x16_f16 v[34:49], v[90:93], v[240:243], v[34:49]
	ds_read_b128 v[170:173], v179 offset:352
	v_pk_fma_f16 v55, v55, s55, v233 op_sel_hi:[1,0,0]
	v_pk_fma_f16 v54, v54, s55, v233 op_sel_hi:[1,0,0]
	v_pk_max_f16 v53, v53, v55
	v_pk_max_f16 v52, v52, v54
	s_waitcnt lgkmcnt(5)
	v_mfma_f32_32x32x16_f16 v[34:49], v[118:121], v[244:247], v[34:49]
	ds_read_b128 v[240:243], v179 offset:384
	v_cvt_pk_f16_f32 v166, v26, v27
	v_cvt_pk_f16_f32 v167, v28, v29
	v_mfma_f32_16x16x32_f16 v[62:65], v[70:73], v[50:53], 0
	s_waitcnt lgkmcnt(5)
	v_mfma_f32_32x32x16_f16 v[34:49], v[78:81], v[18:21], v[34:49]
	ds_read_b128 v[26:29], v179 offset:416
	v_exp_f16_e64 v244, v166 clamp
	v_exp_f16_e64 v245, v167 clamp
	v_exp_f16_sdwa v244, v166 clamp dst_sel:WORD_1 dst_unused:UNUSED_PRESERVE src0_sel:WORD_1
	v_exp_f16_sdwa v245, v167 clamp dst_sel:WORD_1 dst_unused:UNUSED_PRESERVE src0_sel:WORD_1
	s_nop 0
	s_waitcnt lgkmcnt(5)
	v_mfma_f32_32x32x16_f16 v[34:49], v[102:105], v[248:251], v[34:49]
	ds_read_b128 v[18:21], v179 offset:448
	v_pk_fma_f16 v245, v245, s55, v233 op_sel_hi:[1,0,0]
	s_nop 0
	v_pk_max_f16 v245, v167, v245
	v_pk_fma_f16 v167, v244, s55, v233 op_sel_hi:[1,0,0]
	s_nop 0
	v_pk_max_f16 v244, v166, v167
	s_waitcnt lgkmcnt(5)
	v_mfma_f32_32x32x16_f16 v[34:49], v[74:77], v[252:255], v[34:49]
	ds_read_b128 v[248:251], v179 offset:480
	v_cvt_pk_f16_f32 v30, v30, v31
	v_cvt_pk_f16_f32 v31, v32, v33
	s_waitcnt lgkmcnt(5)
	v_mfma_f32_32x32x16_f16 v[34:49], v[106:109], v[22:25], v[34:49]
	v_exp_f16_e64 v32, v30 clamp
	v_exp_f16_e64 v33, v31 clamp
	v_exp_f16_sdwa v32, v30 clamp dst_sel:WORD_1 dst_unused:UNUSED_PRESERVE src0_sel:WORD_1
	v_exp_f16_sdwa v33, v31 clamp dst_sel:WORD_1 dst_unused:UNUSED_PRESERVE src0_sel:WORD_1
	s_nop 0
	s_waitcnt lgkmcnt(4)
	v_mfma_f32_32x32x16_f16 v[34:49], v[82:85], v[170:173], v[34:49]
	v_pk_fma_f16 v22, v33, s55, v233 op_sel_hi:[1,0,0]
	s_nop 0
	v_pk_max_f16 v247, v31, v22
	v_pk_fma_f16 v22, v32, s55, v233 op_sel_hi:[1,0,0]
	s_nop 0
	v_pk_max_f16 v246, v30, v22
	s_waitcnt lgkmcnt(3)
	v_mfma_f32_32x32x16_f16 v[34:49], v[110:113], v[240:243], v[34:49]
	s_waitcnt vmcnt(2)
	v_pk_add_f16 v24, v154, v146
	v_pk_add_f16 v25, v155, v147
	s_nop 0
	v_pk_mul_f16 v22, v156, v148 clamp
	v_pk_mul_f16 v23, v157, v149 clamp
	v_pk_max_f16 v22, v24, v22
	v_pk_max_f16 v23, v25, v23
	ds_write_b64 v189, v[22:23] offset:33792
	v_mfma_f32_16x16x32_f16 v[62:65], v[66:69], v[244:247], v[62:65]
	s_waitcnt lgkmcnt(3)
	v_mfma_f32_32x32x16_f16 v[34:49], v[94:97], v[26:29], v[34:49]
	v_pk_add_f16 v24, v154, v138
	v_pk_add_f16 v25, v155, v139
	s_nop 0
	v_pk_mul_f16 v22, v156, v140 clamp
	v_pk_mul_f16 v23, v157, v141 clamp
	v_pk_max_f16 v22, v24, v22
	v_pk_max_f16 v23, v25, v23
	ds_write_b64 v189, v[22:23] offset:34320
	s_waitcnt lgkmcnt(3)
	v_mfma_f32_32x32x16_f16 v[34:49], v[134:137], v[18:21], v[34:49]
	v_pk_add_f16 v24, v154, v150
	v_pk_add_f16 v25, v155, v151
	s_nop 0
	v_pk_mul_f16 v22, v156, v152 clamp
	v_pk_mul_f16 v23, v157, v153 clamp
	v_pk_max_f16 v22, v24, v22
	v_pk_max_f16 v23, v25, v23
	ds_write_b64 v189, v[22:23] offset:34848
	s_waitcnt lgkmcnt(3)
	v_mfma_f32_32x32x16_f16 v[34:49], v[130:133], v[248:251], v[34:49]
	v_pk_add_f16 v20, v154, v142
	v_pk_add_f16 v21, v155, v143
	s_nop 0
	v_pk_mul_f16 v18, v156, v144 clamp
	v_pk_mul_f16 v19, v157, v145 clamp
	v_pk_max_f16 v18, v20, v18
	v_pk_max_f16 v19, v21, v19
	ds_write_b64 v189, v[18:19] offset:35376
	ds_write2_b32 v229, v62, v63 offset1:1
	s_and_saveexec_b64 s[28:29], s[0:1]
	ds_write2_b32 v229, v64, v65 offset0:2 offset1:3
	s_or_b64 exec, exec, s[28:29]
	v_lshl_add_u64 v[166:167], s[20:21], 4, v[168:169]
	global_load_dwordx4 v[154:157], v[166:167], off
	ds_read_b128 v[50:53], v179 offset:16896
	ds_read_b128 v[54:57], v179 offset:16928
	ds_read_b128 v[58:61], v179 offset:16960
	ds_read_b128 v[62:65], v179 offset:16992
	ds_read_b128 v[168:171], v179 offset:17024
	ds_read_b128 v[240:243], v179 offset:17056
	s_waitcnt lgkmcnt(5)
	v_mfma_f32_32x32x16_f16 v[18:33], v[122:125], v[50:53], v[2:17]
	ds_read_b128 v[244:247], v179 offset:17088
	v_cvt_pk_f16_f32 v172, v34, v35
	v_cvt_pk_f16_f32 v173, v36, v37
	s_waitcnt lgkmcnt(5)
	v_mfma_f32_32x32x16_f16 v[18:33], v[98:101], v[54:57], v[18:33]
	ds_read_b128 v[34:37], v179 offset:17120
	v_exp_f16_e64 v50, v172 clamp
	v_exp_f16_e64 v51, v173 clamp
	v_exp_f16_sdwa v50, v172 clamp dst_sel:WORD_1 dst_unused:UNUSED_PRESERVE src0_sel:WORD_1
	v_exp_f16_sdwa v51, v173 clamp dst_sel:WORD_1 dst_unused:UNUSED_PRESERVE src0_sel:WORD_1
	s_nop 0
	s_waitcnt lgkmcnt(5)
	v_mfma_f32_32x32x16_f16 v[18:33], v[114:117], v[58:61], v[18:33]
	ds_read_b128 v[248:251], v179 offset:17152
	v_pk_fma_f16 v51, v51, s55, v233 op_sel_hi:[1,0,0]
	v_pk_fma_f16 v50, v50, s55, v233 op_sel_hi:[1,0,0]
	v_pk_max_f16 v51, v173, v51
	v_pk_max_f16 v50, v172, v50
	s_waitcnt lgkmcnt(5)
	v_mfma_f32_32x32x16_f16 v[18:33], v[86:89], v[62:65], v[18:33]
	ds_read_b128 v[252:255], v179 offset:17184
	v_cvt_pk_f16_f32 v52, v38, v39
	v_cvt_pk_f16_f32 v53, v40, v41
	s_waitcnt lgkmcnt(5)
	v_mfma_f32_32x32x16_f16 v[18:33], v[126:129], v[168:171], v[18:33]
	ds_read_b128 v[38:41], v179 offset:17216
	v_exp_f16_e64 v54, v52 clamp
	v_exp_f16_e64 v55, v53 clamp
	v_exp_f16_sdwa v54, v52 clamp dst_sel:WORD_1 dst_unused:UNUSED_PRESERVE src0_sel:WORD_1
	v_exp_f16_sdwa v55, v53 clamp dst_sel:WORD_1 dst_unused:UNUSED_PRESERVE src0_sel:WORD_1
	s_nop 0
	s_waitcnt lgkmcnt(5)
	v_mfma_f32_32x32x16_f16 v[18:33], v[90:93], v[240:243], v[18:33]
	ds_read_b128 v[168:171], v179 offset:17248
	v_pk_fma_f16 v55, v55, s55, v233 op_sel_hi:[1,0,0]
	v_pk_fma_f16 v54, v54, s55, v233 op_sel_hi:[1,0,0]
	v_pk_max_f16 v53, v53, v55
	v_pk_max_f16 v52, v52, v54
	s_waitcnt lgkmcnt(5)
	v_mfma_f32_32x32x16_f16 v[18:33], v[118:121], v[244:247], v[18:33]
	ds_read_b128 v[240:243], v179 offset:17280
	v_cvt_pk_f16_f32 v172, v42, v43
	v_cvt_pk_f16_f32 v173, v44, v45
	v_mfma_f32_16x16x32_f16 v[62:65], v[70:73], v[50:53], 0
	s_waitcnt lgkmcnt(5)
	v_mfma_f32_32x32x16_f16 v[18:33], v[78:81], v[34:37], v[18:33]
	ds_read_b128 v[42:45], v179 offset:17312
	v_exp_f16_e64 v244, v172 clamp
	v_exp_f16_e64 v245, v173 clamp
	v_exp_f16_sdwa v244, v172 clamp dst_sel:WORD_1 dst_unused:UNUSED_PRESERVE src0_sel:WORD_1
	v_exp_f16_sdwa v245, v173 clamp dst_sel:WORD_1 dst_unused:UNUSED_PRESERVE src0_sel:WORD_1
	s_nop 0
	s_waitcnt lgkmcnt(5)
	v_mfma_f32_32x32x16_f16 v[18:33], v[102:105], v[248:251], v[18:33]
	ds_read_b128 v[34:37], v179 offset:17344
	v_pk_fma_f16 v245, v245, s55, v233 op_sel_hi:[1,0,0]
	s_nop 0
	v_pk_max_f16 v245, v173, v245
	v_pk_fma_f16 v173, v244, s55, v233 op_sel_hi:[1,0,0]
	s_nop 0
	v_pk_max_f16 v244, v172, v173
	s_waitcnt lgkmcnt(5)
	v_mfma_f32_32x32x16_f16 v[18:33], v[74:77], v[252:255], v[18:33]
	ds_read_b128 v[248:251], v179 offset:17376
	v_cvt_pk_f16_f32 v46, v46, v47
	v_cvt_pk_f16_f32 v47, v48, v49
	s_waitcnt lgkmcnt(5)
	v_mfma_f32_32x32x16_f16 v[18:33], v[106:109], v[38:41], v[18:33]
	v_exp_f16_e64 v48, v46 clamp
	v_exp_f16_e64 v49, v47 clamp
	v_exp_f16_sdwa v48, v46 clamp dst_sel:WORD_1 dst_unused:UNUSED_PRESERVE src0_sel:WORD_1
	v_exp_f16_sdwa v49, v47 clamp dst_sel:WORD_1 dst_unused:UNUSED_PRESERVE src0_sel:WORD_1
	s_nop 0
	s_waitcnt lgkmcnt(4)
	v_mfma_f32_32x32x16_f16 v[18:33], v[82:85], v[168:171], v[18:33]
	v_pk_fma_f16 v38, v49, s55, v233 op_sel_hi:[1,0,0]
	s_nop 0
	v_pk_max_f16 v247, v47, v38
	v_pk_fma_f16 v38, v48, s55, v233 op_sel_hi:[1,0,0]
	s_nop 0
	v_pk_max_f16 v246, v46, v38
	s_waitcnt lgkmcnt(3)
	v_mfma_f32_32x32x16_f16 v[18:33], v[110:113], v[240:243], v[18:33]
	s_waitcnt vmcnt(2)
	v_pk_add_f16 v40, v158, v146
	v_pk_add_f16 v41, v159, v147
	s_nop 0
	v_pk_mul_f16 v38, v160, v148 clamp
	v_pk_mul_f16 v39, v161, v149 clamp
	v_pk_max_f16 v38, v40, v38
	v_pk_max_f16 v39, v41, v39
	ds_write_b64 v189, v[38:39] offset:50688
	v_mfma_f32_16x16x32_f16 v[62:65], v[66:69], v[244:247], v[62:65]
	s_waitcnt lgkmcnt(3)
	v_mfma_f32_32x32x16_f16 v[18:33], v[94:97], v[42:45], v[18:33]
	v_pk_add_f16 v40, v158, v138
	v_pk_add_f16 v41, v159, v139
	s_nop 0
	v_pk_mul_f16 v38, v160, v140 clamp
	v_pk_mul_f16 v39, v161, v141 clamp
	v_pk_max_f16 v38, v40, v38
	v_pk_max_f16 v39, v41, v39
	ds_write_b64 v189, v[38:39] offset:51216
	s_waitcnt lgkmcnt(3)
	v_mfma_f32_32x32x16_f16 v[18:33], v[134:137], v[34:37], v[18:33]
	v_pk_add_f16 v40, v158, v150
	v_pk_add_f16 v41, v159, v151
	s_nop 0
	v_pk_mul_f16 v38, v160, v152 clamp
	v_pk_mul_f16 v39, v161, v153 clamp
	v_pk_max_f16 v38, v40, v38
	v_pk_max_f16 v39, v41, v39
	ds_write_b64 v189, v[38:39] offset:51744
	s_waitcnt lgkmcnt(3)
	v_mfma_f32_32x32x16_f16 v[18:33], v[130:133], v[248:251], v[18:33]
	v_pk_add_f16 v36, v158, v142
	v_pk_add_f16 v37, v159, v143
	s_nop 0
	v_pk_mul_f16 v34, v160, v144 clamp
	v_pk_mul_f16 v35, v161, v145 clamp
	v_pk_max_f16 v34, v36, v34
	v_pk_max_f16 v35, v37, v35
	ds_write_b64 v189, v[34:35] offset:52272
	ds_write2_b32 v206, v62, v63 offset1:1
	s_and_saveexec_b64 s[28:29], s[0:1]
	ds_write2_b32 v206, v64, v65 offset0:2 offset1:3
	s_or_b64 exec, exec, s[28:29]
	s_sub_i32 s28, 0x7d, s31
	s_mul_i32 s28, s28, 6
	s_ashr_i32 s29, s28, 31
	s_add_u32 s26, s26, s28
	s_addc_u32 s27, s27, s29
	s_and_b64 vcc, exec, s[8:9]
	s_waitcnt lgkmcnt(0)
	s_barrier
	ds_read_b128 v[50:53], v179 offset:33792
	ds_read_b128 v[54:57], v179 offset:33824
	ds_read_b128 v[58:61], v179 offset:33856
	ds_read_b128 v[62:65], v179 offset:33888
	s_cbranch_vccnz .LBB1_76
	s_cmp_lg_u32 s41, 0
	s_cbranch_scc0 .LBB1_72
	s_and_saveexec_b64 s[28:29], s[6:7]
	s_cbranch_execz .LBB1_71
	ds_read2_b32 v[34:35], v180 offset1:224
	v_add_u32_e32 v36, 0x700, v180
	ds_read2_b32 v[36:37], v36 offset1:224
	v_add_u32_e32 v38, 0xe00, v180
	s_lshl_b32 s30, s56, 28
	s_waitcnt lgkmcnt(1)
	v_add_f32_e32 v34, 0, v34
	v_add_f32_e32 v40, v34, v35
	ds_read2_b32 v[34:35], v38 offset1:224
	v_add_u32_e32 v38, 0x1500, v180
	ds_read2_b32 v[38:39], v38 offset1:224
	s_waitcnt lgkmcnt(2)
	v_add_f32_e32 v36, v40, v36
	v_add_f32_e32 v36, v36, v37
	s_waitcnt lgkmcnt(1)
	v_add_f32_e32 v34, v36, v34
	s_add_i32 s30, s30, 0xb0000000
	v_add_f32_e32 v34, v34, v35
	s_ashr_i32 s30, s30, 31
	s_waitcnt lgkmcnt(0)
	v_add_f32_e32 v34, v34, v38
	s_and_b32 s30, s30, 0x1800
	v_add_f32_e32 v34, v34, v39
	v_add_u32_e32 v35, s30, v232
	ds_write_b32 v35, v34 offset:384

.LBB1_93:
	v_lshl_add_u64 v[158:159], s[20:21], 4, v[166:167]
	global_load_dwordx4 v[170:173], v[158:159], off
	ds_read_b128 v[166:169], v179 offset:33920
	ds_read_b128 v[240:243], v179 offset:33952
	s_add_i32 s34, s57, 1
	s_waitcnt lgkmcnt(5)
	v_mfma_f32_32x32x16_f16 v[34:49], v[122:125], v[50:53], v[2:17]
	ds_read_b128 v[244:247], v179 offset:33984
	v_cvt_pk_f16_f32 v160, v18, v19
	v_cvt_pk_f16_f32 v161, v20, v21
	s_waitcnt lgkmcnt(5)
	v_mfma_f32_32x32x16_f16 v[34:49], v[98:101], v[54:57], v[34:49]
	ds_read_b128 v[18:21], v179 offset:34016
	v_exp_f16_e64 v50, v160 clamp
	v_exp_f16_e64 v51, v161 clamp
	v_exp_f16_sdwa v50, v160 clamp dst_sel:WORD_1 dst_unused:UNUSED_PRESERVE src0_sel:WORD_1
	v_exp_f16_sdwa v51, v161 clamp dst_sel:WORD_1 dst_unused:UNUSED_PRESERVE src0_sel:WORD_1
	s_nop 0
	s_waitcnt lgkmcnt(5)
	v_mfma_f32_32x32x16_f16 v[34:49], v[114:117], v[58:61], v[34:49]
	ds_read_b128 v[248:251], v179 offset:34048
	v_pk_fma_f16 v51, v51, s55, v233 op_sel_hi:[1,0,0]
	v_pk_fma_f16 v50, v50, s55, v233 op_sel_hi:[1,0,0]
	v_pk_max_f16 v51, v161, v51
	v_pk_max_f16 v50, v160, v50
	s_waitcnt lgkmcnt(5)
	v_mfma_f32_32x32x16_f16 v[34:49], v[86:89], v[62:65], v[34:49]
	ds_read_b128 v[252:255], v179 offset:34080
	v_cvt_pk_f16_f32 v52, v22, v23
	v_cvt_pk_f16_f32 v53, v24, v25
	s_waitcnt lgkmcnt(5)
	v_mfma_f32_32x32x16_f16 v[34:49], v[126:129], v[166:169], v[34:49]
	ds_read_b128 v[22:25], v179 offset:34112
	v_exp_f16_e64 v54, v52 clamp
	v_exp_f16_e64 v55, v53 clamp
	v_exp_f16_sdwa v54, v52 clamp dst_sel:WORD_1 dst_unused:UNUSED_PRESERVE src0_sel:WORD_1
	v_exp_f16_sdwa v55, v53 clamp dst_sel:WORD_1 dst_unused:UNUSED_PRESERVE src0_sel:WORD_1
	s_nop 0
	s_waitcnt lgkmcnt(5)
	v_mfma_f32_32x32x16_f16 v[34:49], v[90:93], v[240:243], v[34:49]
	ds_read_b128 v[166:169], v179 offset:34144
	v_pk_fma_f16 v55, v55, s55, v233 op_sel_hi:[1,0,0]
	v_pk_fma_f16 v54, v54, s55, v233 op_sel_hi:[1,0,0]
	v_pk_max_f16 v53, v53, v55
	v_pk_max_f16 v52, v52, v54
	s_waitcnt lgkmcnt(5)
	v_mfma_f32_32x32x16_f16 v[34:49], v[118:121], v[244:247], v[34:49]
	ds_read_b128 v[240:243], v179 offset:34176
	v_cvt_pk_f16_f32 v160, v26, v27
	v_cvt_pk_f16_f32 v161, v28, v29
	v_mfma_f32_16x16x32_f16 v[62:65], v[70:73], v[50:53], 0
	s_waitcnt lgkmcnt(5)
	v_mfma_f32_32x32x16_f16 v[34:49], v[78:81], v[18:21], v[34:49]
	ds_read_b128 v[26:29], v179 offset:34208
	v_exp_f16_e64 v244, v160 clamp
	v_exp_f16_e64 v245, v161 clamp
	v_exp_f16_sdwa v244, v160 clamp dst_sel:WORD_1 dst_unused:UNUSED_PRESERVE src0_sel:WORD_1
	v_exp_f16_sdwa v245, v161 clamp dst_sel:WORD_1 dst_unused:UNUSED_PRESERVE src0_sel:WORD_1
	s_nop 0
	s_waitcnt lgkmcnt(5)
	v_mfma_f32_32x32x16_f16 v[34:49], v[102:105], v[248:251], v[34:49]
	ds_read_b128 v[18:21], v179 offset:34240
	v_pk_fma_f16 v245, v245, s55, v233 op_sel_hi:[1,0,0]
	s_nop 0
	v_pk_max_f16 v245, v161, v245
	v_pk_fma_f16 v161, v244, s55, v233 op_sel_hi:[1,0,0]
	s_nop 0
	v_pk_max_f16 v244, v160, v161
	s_waitcnt lgkmcnt(5)
	v_mfma_f32_32x32x16_f16 v[34:49], v[74:77], v[252:255], v[34:49]
	ds_read_b128 v[248:251], v179 offset:34272
	v_cvt_pk_f16_f32 v30, v30, v31
	v_cvt_pk_f16_f32 v31, v32, v33
	s_waitcnt lgkmcnt(5)
	v_mfma_f32_32x32x16_f16 v[34:49], v[106:109], v[22:25], v[34:49]
	v_exp_f16_e64 v32, v30 clamp
	v_exp_f16_e64 v33, v31 clamp
	v_exp_f16_sdwa v32, v30 clamp dst_sel:WORD_1 dst_unused:UNUSED_PRESERVE src0_sel:WORD_1
	v_exp_f16_sdwa v33, v31 clamp dst_sel:WORD_1 dst_unused:UNUSED_PRESERVE src0_sel:WORD_1
	s_nop 0
	s_waitcnt lgkmcnt(4)
	v_mfma_f32_32x32x16_f16 v[34:49], v[82:85], v[166:169], v[34:49]
	v_pk_fma_f16 v22, v33, s55, v233 op_sel_hi:[1,0,0]
	s_nop 0
	v_pk_max_f16 v247, v31, v22
	v_pk_fma_f16 v22, v32, s55, v233 op_sel_hi:[1,0,0]
	s_nop 0
	v_pk_max_f16 v246, v30, v22
	s_waitcnt lgkmcnt(3)
	v_mfma_f32_32x32x16_f16 v[34:49], v[110:113], v[240:243], v[34:49]
	s_waitcnt vmcnt(2)
	v_pk_add_f16 v24, v146, v162
	v_pk_add_f16 v25, v147, v163
	s_nop 0
	v_pk_mul_f16 v22, v164, v148 clamp
	v_pk_mul_f16 v23, v165, v149 clamp
	v_pk_max_f16 v22, v24, v22
	v_pk_max_f16 v23, v25, v23
	ds_write_b64 v189, v[22:23]
	v_mfma_f32_16x16x32_f16 v[62:65], v[66:69], v[244:247], v[62:65]
	s_waitcnt lgkmcnt(3)
	v_mfma_f32_32x32x16_f16 v[34:49], v[94:97], v[26:29], v[34:49]
	v_pk_add_f16 v24, v138, v162
	v_pk_add_f16 v25, v139, v163
	s_nop 0
	v_pk_mul_f16 v22, v164, v140 clamp
	v_pk_mul_f16 v23, v165, v141 clamp
	v_pk_max_f16 v22, v24, v22
	v_pk_max_f16 v23, v25, v23
	ds_write_b64 v189, v[22:23] offset:528
	s_waitcnt lgkmcnt(3)
	v_mfma_f32_32x32x16_f16 v[34:49], v[134:137], v[18:21], v[34:49]
	v_pk_add_f16 v24, v150, v162
	v_pk_add_f16 v25, v151, v163
	s_nop 0
	v_pk_mul_f16 v22, v164, v152 clamp
	v_pk_mul_f16 v23, v165, v153 clamp
	v_pk_max_f16 v22, v24, v22
	v_pk_max_f16 v23, v25, v23
	ds_write_b64 v189, v[22:23] offset:1056
	s_waitcnt lgkmcnt(3)
	v_mfma_f32_32x32x16_f16 v[34:49], v[130:133], v[248:251], v[34:49]
	s_waitcnt vmcnt(1)
	v_pk_add_f16 v20, v142, v162
	v_pk_add_f16 v21, v143, v163
	s_nop 0
	v_pk_mul_f16 v18, v164, v144 clamp
	v_pk_mul_f16 v19, v165, v145 clamp
	v_pk_max_f16 v18, v20, v18
	v_pk_max_f16 v19, v21, v19
	ds_write_b64 v189, v[18:19] offset:1584
	ds_write2_b32 v201, v62, v63 offset1:1
	s_and_saveexec_b64 s[30:31], s[0:1]
	ds_write2_b32 v201, v64, v65 offset0:2 offset1:3
	s_or_b64 exec, exec, s[30:31]
	v_lshl_add_u64 v[158:159], s[20:21], 4, v[158:159]
	global_load_dwordx4 v[166:169], v[158:159], off
	ds_read_b128 v[50:53], v179 offset:50688
	ds_read_b128 v[54:57], v179 offset:50720
	ds_read_b128 v[58:61], v179 offset:50752
	ds_read_b128 v[62:65], v179 offset:50784
	ds_read_b128 v[160:163], v179 offset:50816
	ds_read_b128 v[240:243], v179 offset:50848
	s_waitcnt lgkmcnt(5)
	v_mfma_f32_32x32x16_f16 v[18:33], v[122:125], v[50:53], v[2:17]
	ds_read_b128 v[244:247], v179 offset:50880
	v_cvt_pk_f16_f32 v164, v34, v35
	v_cvt_pk_f16_f32 v165, v36, v37
	s_waitcnt lgkmcnt(5)
	v_mfma_f32_32x32x16_f16 v[18:33], v[98:101], v[54:57], v[18:33]
	ds_read_b128 v[34:37], v179 offset:50912
	v_exp_f16_e64 v50, v164 clamp
	v_exp_f16_e64 v51, v165 clamp
	v_exp_f16_sdwa v50, v164 clamp dst_sel:WORD_1 dst_unused:UNUSED_PRESERVE src0_sel:WORD_1
	v_exp_f16_sdwa v51, v165 clamp dst_sel:WORD_1 dst_unused:UNUSED_PRESERVE src0_sel:WORD_1
	s_nop 0
	s_waitcnt lgkmcnt(5)
	v_mfma_f32_32x32x16_f16 v[18:33], v[114:117], v[58:61], v[18:33]
	ds_read_b128 v[248:251], v179 offset:50944
	v_pk_fma_f16 v51, v51, s55, v233 op_sel_hi:[1,0,0]
	v_pk_fma_f16 v50, v50, s55, v233 op_sel_hi:[1,0,0]
	v_pk_max_f16 v51, v165, v51
	v_pk_max_f16 v50, v164, v50
	s_waitcnt lgkmcnt(5)
	v_mfma_f32_32x32x16_f16 v[18:33], v[86:89], v[62:65], v[18:33]
	ds_read_b128 v[252:255], v179 offset:50976
	v_cvt_pk_f16_f32 v52, v38, v39
	v_cvt_pk_f16_f32 v53, v40, v41
	s_waitcnt lgkmcnt(5)
	v_mfma_f32_32x32x16_f16 v[18:33], v[126:129], v[160:163], v[18:33]
	ds_read_b128 v[38:41], v179 offset:51008
	v_exp_f16_e64 v54, v52 clamp
	v_exp_f16_e64 v55, v53 clamp
	v_exp_f16_sdwa v54, v52 clamp dst_sel:WORD_1 dst_unused:UNUSED_PRESERVE src0_sel:WORD_1
	v_exp_f16_sdwa v55, v53 clamp dst_sel:WORD_1 dst_unused:UNUSED_PRESERVE src0_sel:WORD_1
	s_nop 0
	s_waitcnt lgkmcnt(5)
	v_mfma_f32_32x32x16_f16 v[18:33], v[90:93], v[240:243], v[18:33]
	ds_read_b128 v[160:163], v179 offset:51040
	v_pk_fma_f16 v55, v55, s55, v233 op_sel_hi:[1,0,0]
	v_pk_fma_f16 v54, v54, s55, v233 op_sel_hi:[1,0,0]
	v_pk_max_f16 v53, v53, v55
	v_pk_max_f16 v52, v52, v54
	s_waitcnt lgkmcnt(5)
	v_mfma_f32_32x32x16_f16 v[18:33], v[118:121], v[244:247], v[18:33]
	ds_read_b128 v[240:243], v179 offset:51072
	v_cvt_pk_f16_f32 v164, v42, v43
	v_cvt_pk_f16_f32 v165, v44, v45
	v_mfma_f32_16x16x32_f16 v[62:65], v[70:73], v[50:53], 0
	s_waitcnt lgkmcnt(5)
	v_mfma_f32_32x32x16_f16 v[18:33], v[78:81], v[34:37], v[18:33]
	ds_read_b128 v[42:45], v179 offset:51104
	v_exp_f16_e64 v244, v164 clamp
	v_exp_f16_e64 v245, v165 clamp
	v_exp_f16_sdwa v244, v164 clamp dst_sel:WORD_1 dst_unused:UNUSED_PRESERVE src0_sel:WORD_1
	v_exp_f16_sdwa v245, v165 clamp dst_sel:WORD_1 dst_unused:UNUSED_PRESERVE src0_sel:WORD_1
	s_nop 0
	s_waitcnt lgkmcnt(5)
	v_mfma_f32_32x32x16_f16 v[18:33], v[102:105], v[248:251], v[18:33]
	ds_read_b128 v[34:37], v179 offset:51136
	v_pk_fma_f16 v245, v245, s55, v233 op_sel_hi:[1,0,0]
	s_nop 0
	v_pk_max_f16 v245, v165, v245
	v_pk_fma_f16 v165, v244, s55, v233 op_sel_hi:[1,0,0]
	s_nop 0
	v_pk_max_f16 v244, v164, v165
	s_waitcnt lgkmcnt(5)
	v_mfma_f32_32x32x16_f16 v[18:33], v[74:77], v[252:255], v[18:33]
	ds_read_b128 v[248:251], v179 offset:51168
	v_cvt_pk_f16_f32 v46, v46, v47
	v_cvt_pk_f16_f32 v47, v48, v49
	s_waitcnt lgkmcnt(5)
	v_mfma_f32_32x32x16_f16 v[18:33], v[106:109], v[38:41], v[18:33]
	v_exp_f16_e64 v48, v46 clamp
	v_exp_f16_e64 v49, v47 clamp
	v_exp_f16_sdwa v48, v46 clamp dst_sel:WORD_1 dst_unused:UNUSED_PRESERVE src0_sel:WORD_1
	v_exp_f16_sdwa v49, v47 clamp dst_sel:WORD_1 dst_unused:UNUSED_PRESERVE src0_sel:WORD_1
	s_nop 0
	s_waitcnt lgkmcnt(4)
	v_mfma_f32_32x32x16_f16 v[18:33], v[82:85], v[160:163], v[18:33]
	v_pk_fma_f16 v38, v49, s55, v233 op_sel_hi:[1,0,0]
	s_nop 0
	v_pk_max_f16 v247, v47, v38
	v_pk_fma_f16 v38, v48, s55, v233 op_sel_hi:[1,0,0]
	s_nop 0
	v_pk_max_f16 v246, v46, v38
	s_waitcnt lgkmcnt(3)
	v_mfma_f32_32x32x16_f16 v[18:33], v[110:113], v[240:243], v[18:33]
	v_pk_add_f16 v40, v146, v154
	v_pk_add_f16 v41, v147, v155
	s_nop 0
	v_pk_mul_f16 v38, v156, v148 clamp
	v_pk_mul_f16 v39, v157, v149 clamp
	v_pk_max_f16 v38, v40, v38
	v_pk_max_f16 v39, v41, v39
	ds_write_b64 v189, v[38:39] offset:16896
	v_mfma_f32_16x16x32_f16 v[62:65], v[66:69], v[244:247], v[62:65]
	s_waitcnt lgkmcnt(3)
	v_mfma_f32_32x32x16_f16 v[18:33], v[94:97], v[42:45], v[18:33]
	v_pk_add_f16 v40, v138, v154
	v_pk_add_f16 v41, v139, v155
	s_nop 0
	v_pk_mul_f16 v38, v156, v140 clamp
	v_pk_mul_f16 v39, v157, v141 clamp
	v_pk_max_f16 v38, v40, v38
	v_pk_max_f16 v39, v41, v39
	ds_write_b64 v189, v[38:39] offset:17424
	s_waitcnt lgkmcnt(3)
	v_mfma_f32_32x32x16_f16 v[18:33], v[134:137], v[34:37], v[18:33]
	v_pk_add_f16 v40, v150, v154
	v_pk_add_f16 v41, v151, v155
	s_nop 0
	v_pk_mul_f16 v38, v156, v152 clamp
	v_pk_mul_f16 v39, v157, v153 clamp
	v_pk_max_f16 v38, v40, v38
	v_pk_max_f16 v39, v41, v39
	ds_write_b64 v189, v[38:39] offset:17952
	s_waitcnt lgkmcnt(3)
	v_mfma_f32_32x32x16_f16 v[18:33], v[130:133], v[248:251], v[18:33]
	v_pk_add_f16 v36, v142, v154
	v_pk_add_f16 v37, v143, v155
	s_nop 0
	v_pk_mul_f16 v34, v156, v144 clamp
	v_pk_mul_f16 v35, v157, v145 clamp
	v_pk_max_f16 v34, v36, v34
	v_pk_max_f16 v35, v37, v35
	ds_write_b64 v189, v[34:35] offset:18480
	ds_write2_b32 v211, v62, v63 offset1:1
	s_and_saveexec_b64 s[30:31], s[0:1]
	ds_write2_b32 v211, v64, v65 offset0:2 offset1:3
	s_or_b64 exec, exec, s[30:31]
	s_sub_i32 s30, 0x7d, s34
	s_mul_i32 s30, s30, 6
	s_ashr_i32 s31, s30, 31
	s_add_u32 s28, s28, s30
	s_addc_u32 s29, s29, s31
	s_and_b64 vcc, exec, s[8:9]
	s_waitcnt lgkmcnt(0)
	s_barrier
	ds_read_b128 v[50:53], v179
	ds_read_b128 v[54:57], v179 offset:32
	ds_read_b128 v[58:61], v179 offset:64
	ds_read_b128 v[62:65], v179 offset:96
	ds_read_b128 v[162:165], v179 offset:128
	ds_read_b128 v[240:243], v179 offset:160
	s_cbranch_vccnz .LBB1_110
	s_cmp_eq_u32 s41, 0
	s_cbranch_scc1 .LBB1_106
	s_and_saveexec_b64 s[30:31], s[6:7]
	s_cbranch_execz .LBB1_105
	ds_read2_b32 v[34:35], v200 offset1:224
	ds_read2_b32 v[36:37], v234 offset1:224
	ds_read2_b32 v[38:39], v235 offset1:224
	ds_read2_b32 v[40:41], v236 offset1:224
	s_lshl_b32 s35, s56, 28
	s_add_i32 s35, s35, 0xd0000000
	s_ashr_i32 s35, s35, 31
	s_waitcnt lgkmcnt(3)
	v_add_f32_e32 v34, 0, v34
	v_add_f32_e32 v34, v34, v35
	s_waitcnt lgkmcnt(2)
	v_add_f32_e32 v34, v34, v36
	v_add_f32_e32 v34, v34, v37
	s_waitcnt lgkmcnt(1)
	v_add_f32_e32 v34, v34, v38
	v_add_f32_e32 v34, v34, v39
	s_waitcnt lgkmcnt(0)
	v_add_f32_e32 v34, v34, v40
	s_and_b32 s35, s35, 0x1800
	v_add_f32_e32 v34, v34, v41
	v_add_u32_e32 v35, s35, v232
	ds_write_b32 v35, v34 offset:640

.LBB1_119:
	v_lshl_add_u64 v[154:155], s[20:21], 4, v[158:159]
	global_load_dwordx4 v[158:161], v[154:155], off
	s_waitcnt lgkmcnt(5)
	v_mfma_f32_32x32x16_f16 v[34:49], v[122:125], v[50:53], v[2:17]
	ds_read_b128 v[244:247], v179 offset:192
	v_cvt_pk_f16_f32 v156, v18, v19
	v_cvt_pk_f16_f32 v157, v20, v21
	s_waitcnt lgkmcnt(5)
	v_mfma_f32_32x32x16_f16 v[34:49], v[98:101], v[54:57], v[34:49]
	ds_read_b128 v[18:21], v179 offset:224
	v_exp_f16_e64 v50, v156 clamp
	v_exp_f16_e64 v51, v157 clamp
	v_exp_f16_sdwa v50, v156 clamp dst_sel:WORD_1 dst_unused:UNUSED_PRESERVE src0_sel:WORD_1
	v_exp_f16_sdwa v51, v157 clamp dst_sel:WORD_1 dst_unused:UNUSED_PRESERVE src0_sel:WORD_1
	s_nop 0
	s_waitcnt lgkmcnt(5)
	v_mfma_f32_32x32x16_f16 v[34:49], v[114:117], v[58:61], v[34:49]
	ds_read_b128 v[248:251], v179 offset:256
	v_pk_fma_f16 v51, v51, s55, v233 op_sel_hi:[1,0,0]
	v_pk_fma_f16 v50, v50, s55, v233 op_sel_hi:[1,0,0]
	v_pk_max_f16 v51, v157, v51
	v_pk_max_f16 v50, v156, v50
	s_waitcnt lgkmcnt(5)
	v_mfma_f32_32x32x16_f16 v[34:49], v[86:89], v[62:65], v[34:49]
	ds_read_b128 v[252:255], v179 offset:288
	v_cvt_pk_f16_f32 v52, v22, v23
	v_cvt_pk_f16_f32 v53, v24, v25
	s_waitcnt lgkmcnt(5)
	v_mfma_f32_32x32x16_f16 v[34:49], v[126:129], v[162:165], v[34:49]
	ds_read_b128 v[22:25], v179 offset:320
	v_exp_f16_e64 v54, v52 clamp
	v_exp_f16_e64 v55, v53 clamp
	v_exp_f16_sdwa v54, v52 clamp dst_sel:WORD_1 dst_unused:UNUSED_PRESERVE src0_sel:WORD_1
	v_exp_f16_sdwa v55, v53 clamp dst_sel:WORD_1 dst_unused:UNUSED_PRESERVE src0_sel:WORD_1
	s_nop 0
	s_waitcnt lgkmcnt(5)
	v_mfma_f32_32x32x16_f16 v[34:49], v[90:93], v[240:243], v[34:49]
	ds_read_b128 v[162:165], v179 offset:352
	v_pk_fma_f16 v55, v55, s55, v233 op_sel_hi:[1,0,0]
	v_pk_fma_f16 v54, v54, s55, v233 op_sel_hi:[1,0,0]
	v_pk_max_f16 v53, v53, v55
	v_pk_max_f16 v52, v52, v54
	s_waitcnt lgkmcnt(5)
	v_mfma_f32_32x32x16_f16 v[34:49], v[118:121], v[244:247], v[34:49]
	ds_read_b128 v[240:243], v179 offset:384
	v_cvt_pk_f16_f32 v156, v26, v27
	v_cvt_pk_f16_f32 v157, v28, v29
	v_mfma_f32_16x16x32_f16 v[62:65], v[70:73], v[50:53], 0
	s_waitcnt lgkmcnt(5)
	v_mfma_f32_32x32x16_f16 v[34:49], v[78:81], v[18:21], v[34:49]
	ds_read_b128 v[26:29], v179 offset:416
	v_exp_f16_e64 v244, v156 clamp
	v_exp_f16_e64 v245, v157 clamp
	v_exp_f16_sdwa v244, v156 clamp dst_sel:WORD_1 dst_unused:UNUSED_PRESERVE src0_sel:WORD_1
	v_exp_f16_sdwa v245, v157 clamp dst_sel:WORD_1 dst_unused:UNUSED_PRESERVE src0_sel:WORD_1
	s_nop 0
	s_waitcnt lgkmcnt(5)
	v_mfma_f32_32x32x16_f16 v[34:49], v[102:105], v[248:251], v[34:49]
	ds_read_b128 v[18:21], v179 offset:448
	v_pk_fma_f16 v245, v245, s55, v233 op_sel_hi:[1,0,0]
	s_nop 0
	v_pk_max_f16 v245, v157, v245
	v_pk_fma_f16 v157, v244, s55, v233 op_sel_hi:[1,0,0]
	s_nop 0
	v_pk_max_f16 v244, v156, v157
	s_waitcnt lgkmcnt(5)
	v_mfma_f32_32x32x16_f16 v[34:49], v[74:77], v[252:255], v[34:49]
	ds_read_b128 v[248:251], v179 offset:480
	v_cvt_pk_f16_f32 v30, v30, v31
	v_cvt_pk_f16_f32 v31, v32, v33
	s_waitcnt lgkmcnt(5)
	v_mfma_f32_32x32x16_f16 v[34:49], v[106:109], v[22:25], v[34:49]
	v_exp_f16_e64 v32, v30 clamp
	v_exp_f16_e64 v33, v31 clamp
	v_exp_f16_sdwa v32, v30 clamp dst_sel:WORD_1 dst_unused:UNUSED_PRESERVE src0_sel:WORD_1
	v_exp_f16_sdwa v33, v31 clamp dst_sel:WORD_1 dst_unused:UNUSED_PRESERVE src0_sel:WORD_1
	s_nop 0
	s_waitcnt lgkmcnt(4)
	v_mfma_f32_32x32x16_f16 v[34:49], v[82:85], v[162:165], v[34:49]
	v_pk_fma_f16 v22, v33, s55, v233 op_sel_hi:[1,0,0]
	s_nop 0
	v_pk_max_f16 v247, v31, v22
	v_pk_fma_f16 v22, v32, s55, v233 op_sel_hi:[1,0,0]
	s_nop 0
	v_pk_max_f16 v246, v30, v22
	s_waitcnt lgkmcnt(3)
	v_mfma_f32_32x32x16_f16 v[34:49], v[110:113], v[240:243], v[34:49]
	s_waitcnt vmcnt(2)
	v_pk_add_f16 v24, v170, v146
	v_pk_add_f16 v25, v171, v147
	s_nop 0
	v_pk_mul_f16 v22, v172, v148 clamp
	v_pk_mul_f16 v23, v173, v149 clamp
	v_pk_max_f16 v22, v24, v22
	v_pk_max_f16 v23, v25, v23
	ds_write_b64 v189, v[22:23] offset:33792
	v_mfma_f32_16x16x32_f16 v[62:65], v[66:69], v[244:247], v[62:65]
	s_waitcnt lgkmcnt(3)
	v_mfma_f32_32x32x16_f16 v[34:49], v[94:97], v[26:29], v[34:49]
	v_pk_add_f16 v24, v170, v138
	v_pk_add_f16 v25, v171, v139
	s_nop 0
	v_pk_mul_f16 v22, v172, v140 clamp
	v_pk_mul_f16 v23, v173, v141 clamp
	v_pk_max_f16 v22, v24, v22
	v_pk_max_f16 v23, v25, v23
	ds_write_b64 v189, v[22:23] offset:34320
	s_waitcnt lgkmcnt(3)
	v_mfma_f32_32x32x16_f16 v[34:49], v[134:137], v[18:21], v[34:49]
	v_pk_add_f16 v24, v170, v150
	v_pk_add_f16 v25, v171, v151
	s_nop 0
	v_pk_mul_f16 v22, v172, v152 clamp
	v_pk_mul_f16 v23, v173, v153 clamp
	v_pk_max_f16 v22, v24, v22
	v_pk_max_f16 v23, v25, v23
	ds_write_b64 v189, v[22:23] offset:34848
	s_waitcnt lgkmcnt(3)
	v_mfma_f32_32x32x16_f16 v[34:49], v[130:133], v[248:251], v[34:49]
	v_pk_add_f16 v20, v170, v142
	v_pk_add_f16 v21, v171, v143
	s_nop 0
	v_pk_mul_f16 v18, v172, v144 clamp
	v_pk_mul_f16 v19, v173, v145 clamp
	v_pk_max_f16 v18, v20, v18
	v_pk_max_f16 v19, v21, v19
	ds_write_b64 v189, v[18:19] offset:35376
	ds_write2_b32 v229, v62, v63 offset1:1
	s_and_saveexec_b64 s[30:31], s[0:1]
	ds_write2_b32 v229, v64, v65 offset0:2 offset1:3
	s_or_b64 exec, exec, s[30:31]
	v_lshl_add_u64 v[154:155], s[20:21], 4, v[154:155]
	global_load_dwordx4 v[162:165], v[154:155], off
	ds_read_b128 v[50:53], v179 offset:16896
	ds_read_b128 v[54:57], v179 offset:16928
	ds_read_b128 v[58:61], v179 offset:16960
	ds_read_b128 v[62:65], v179 offset:16992
	ds_read_b128 v[170:173], v179 offset:17024
	ds_read_b128 v[240:243], v179 offset:17056
	s_waitcnt lgkmcnt(5)
	v_mfma_f32_32x32x16_f16 v[18:33], v[122:125], v[50:53], v[2:17]
	ds_read_b128 v[244:247], v179 offset:17088
	v_cvt_pk_f16_f32 v156, v34, v35
	v_cvt_pk_f16_f32 v157, v36, v37
	s_waitcnt lgkmcnt(5)
	v_mfma_f32_32x32x16_f16 v[18:33], v[98:101], v[54:57], v[18:33]
	ds_read_b128 v[34:37], v179 offset:17120
	v_exp_f16_e64 v50, v156 clamp
	v_exp_f16_e64 v51, v157 clamp
	v_exp_f16_sdwa v50, v156 clamp dst_sel:WORD_1 dst_unused:UNUSED_PRESERVE src0_sel:WORD_1
	v_exp_f16_sdwa v51, v157 clamp dst_sel:WORD_1 dst_unused:UNUSED_PRESERVE src0_sel:WORD_1
	s_nop 0
	s_waitcnt lgkmcnt(5)
	v_mfma_f32_32x32x16_f16 v[18:33], v[114:117], v[58:61], v[18:33]
	ds_read_b128 v[248:251], v179 offset:17152
	v_pk_fma_f16 v51, v51, s55, v233 op_sel_hi:[1,0,0]
	v_pk_fma_f16 v50, v50, s55, v233 op_sel_hi:[1,0,0]
	v_pk_max_f16 v51, v157, v51
	v_pk_max_f16 v50, v156, v50
	s_waitcnt lgkmcnt(5)
	v_mfma_f32_32x32x16_f16 v[18:33], v[86:89], v[62:65], v[18:33]
	ds_read_b128 v[252:255], v179 offset:17184
	v_cvt_pk_f16_f32 v52, v38, v39
	v_cvt_pk_f16_f32 v53, v40, v41
	s_waitcnt lgkmcnt(5)
	v_mfma_f32_32x32x16_f16 v[18:33], v[126:129], v[170:173], v[18:33]
	ds_read_b128 v[38:41], v179 offset:17216
	v_exp_f16_e64 v54, v52 clamp
	v_exp_f16_e64 v55, v53 clamp
	v_exp_f16_sdwa v54, v52 clamp dst_sel:WORD_1 dst_unused:UNUSED_PRESERVE src0_sel:WORD_1
	v_exp_f16_sdwa v55, v53 clamp dst_sel:WORD_1 dst_unused:UNUSED_PRESERVE src0_sel:WORD_1
	s_nop 0
	s_waitcnt lgkmcnt(5)
	v_mfma_f32_32x32x16_f16 v[18:33], v[90:93], v[240:243], v[18:33]
	ds_read_b128 v[170:173], v179 offset:17248
	v_pk_fma_f16 v55, v55, s55, v233 op_sel_hi:[1,0,0]
	v_pk_fma_f16 v54, v54, s55, v233 op_sel_hi:[1,0,0]
	v_pk_max_f16 v53, v53, v55
	v_pk_max_f16 v52, v52, v54
	s_waitcnt lgkmcnt(5)
	v_mfma_f32_32x32x16_f16 v[18:33], v[118:121], v[244:247], v[18:33]
	ds_read_b128 v[240:243], v179 offset:17280
	v_cvt_pk_f16_f32 v156, v42, v43
	v_cvt_pk_f16_f32 v157, v44, v45
	v_mfma_f32_16x16x32_f16 v[62:65], v[70:73], v[50:53], 0
	s_waitcnt lgkmcnt(5)
	v_mfma_f32_32x32x16_f16 v[18:33], v[78:81], v[34:37], v[18:33]
	ds_read_b128 v[42:45], v179 offset:17312
	v_exp_f16_e64 v244, v156 clamp
	v_exp_f16_e64 v245, v157 clamp
	v_exp_f16_sdwa v244, v156 clamp dst_sel:WORD_1 dst_unused:UNUSED_PRESERVE src0_sel:WORD_1
	v_exp_f16_sdwa v245, v157 clamp dst_sel:WORD_1 dst_unused:UNUSED_PRESERVE src0_sel:WORD_1
	s_nop 0
	s_waitcnt lgkmcnt(5)
	v_mfma_f32_32x32x16_f16 v[18:33], v[102:105], v[248:251], v[18:33]
	ds_read_b128 v[34:37], v179 offset:17344
	v_pk_fma_f16 v245, v245, s55, v233 op_sel_hi:[1,0,0]
	s_nop 0
	v_pk_max_f16 v245, v157, v245
	v_pk_fma_f16 v157, v244, s55, v233 op_sel_hi:[1,0,0]
	s_nop 0
	v_pk_max_f16 v244, v156, v157
	s_waitcnt lgkmcnt(5)
	v_mfma_f32_32x32x16_f16 v[18:33], v[74:77], v[252:255], v[18:33]
	ds_read_b128 v[248:251], v179 offset:17376
	v_cvt_pk_f16_f32 v46, v46, v47
	v_cvt_pk_f16_f32 v47, v48, v49
	s_waitcnt lgkmcnt(5)
	v_mfma_f32_32x32x16_f16 v[18:33], v[106:109], v[38:41], v[18:33]
	v_exp_f16_e64 v48, v46 clamp
	v_exp_f16_e64 v49, v47 clamp
	v_exp_f16_sdwa v48, v46 clamp dst_sel:WORD_1 dst_unused:UNUSED_PRESERVE src0_sel:WORD_1
	v_exp_f16_sdwa v49, v47 clamp dst_sel:WORD_1 dst_unused:UNUSED_PRESERVE src0_sel:WORD_1
	s_nop 0
	s_waitcnt lgkmcnt(4)
	v_mfma_f32_32x32x16_f16 v[18:33], v[82:85], v[170:173], v[18:33]
	v_pk_fma_f16 v38, v49, s55, v233 op_sel_hi:[1,0,0]
	s_nop 0
	v_pk_max_f16 v247, v47, v38
	v_pk_fma_f16 v38, v48, s55, v233 op_sel_hi:[1,0,0]
	s_nop 0
	v_pk_max_f16 v246, v46, v38
	s_waitcnt lgkmcnt(3)
	v_mfma_f32_32x32x16_f16 v[18:33], v[110:113], v[240:243], v[18:33]
	s_waitcnt vmcnt(2)
	v_pk_add_f16 v40, v166, v146
	v_pk_add_f16 v41, v167, v147
	s_nop 0
	v_pk_mul_f16 v38, v168, v148 clamp
	v_pk_mul_f16 v39, v169, v149 clamp
	v_pk_max_f16 v38, v40, v38
	v_pk_max_f16 v39, v41, v39
	ds_write_b64 v189, v[38:39] offset:50688
	v_mfma_f32_16x16x32_f16 v[62:65], v[66:69], v[244:247], v[62:65]
	s_waitcnt lgkmcnt(3)
	v_mfma_f32_32x32x16_f16 v[18:33], v[94:97], v[42:45], v[18:33]
	v_pk_add_f16 v40, v166, v138
	v_pk_add_f16 v41, v167, v139
	s_nop 0
	v_pk_mul_f16 v38, v168, v140 clamp
	v_pk_mul_f16 v39, v169, v141 clamp
	v_pk_max_f16 v38, v40, v38
	v_pk_max_f16 v39, v41, v39
	ds_write_b64 v189, v[38:39] offset:51216
	s_waitcnt lgkmcnt(3)
	v_mfma_f32_32x32x16_f16 v[18:33], v[134:137], v[34:37], v[18:33]
	v_pk_add_f16 v40, v166, v150
	v_pk_add_f16 v41, v167, v151
	s_nop 0
	v_pk_mul_f16 v38, v168, v152 clamp
	v_pk_mul_f16 v39, v169, v153 clamp
	v_pk_max_f16 v38, v40, v38
	v_pk_max_f16 v39, v41, v39
	ds_write_b64 v189, v[38:39] offset:51744
	s_waitcnt lgkmcnt(3)
	v_mfma_f32_32x32x16_f16 v[18:33], v[130:133], v[248:251], v[18:33]
	v_pk_add_f16 v36, v166, v142
	v_pk_add_f16 v37, v167, v143
	s_nop 0
	v_pk_mul_f16 v34, v168, v144 clamp
	v_pk_mul_f16 v35, v169, v145 clamp
	v_pk_max_f16 v34, v36, v34
	v_pk_max_f16 v35, v37, v35
	ds_write_b64 v189, v[34:35] offset:52272
	ds_write2_b32 v206, v62, v63 offset1:1
	s_and_saveexec_b64 s[30:31], s[0:1]
	ds_write2_b32 v206, v64, v65 offset0:2 offset1:3
	s_or_b64 exec, exec, s[30:31]
	s_add_i32 s34, s34, 1
	s_sub_i32 s30, 0x7d, s34
	s_mul_i32 s30, s30, 6
	s_ashr_i32 s31, s30, 31
	s_add_u32 s28, s28, s30
	s_addc_u32 s29, s29, s31
	s_and_b64 vcc, exec, s[8:9]
	s_waitcnt lgkmcnt(0)
	s_barrier
	ds_read_b128 v[50:53], v179 offset:33792
	ds_read_b128 v[54:57], v179 offset:33824
	ds_read_b128 v[58:61], v179 offset:33856
	ds_read_b128 v[62:65], v179 offset:33888
	ds_read_b128 v[168:171], v179 offset:33920
	ds_read_b128 v[240:243], v179 offset:33952
	s_cbranch_vccnz .LBB1_136
	s_cmp_eq_u32 s41, 0
	s_cbranch_scc1 .LBB1_132
	s_and_saveexec_b64 s[30:31], s[6:7]
	s_cbranch_execz .LBB1_131
	ds_read2_b32 v[34:35], v180 offset1:224
	v_add_u32_e32 v36, 0x700, v180
	ds_read2_b32 v[36:37], v36 offset1:224
	v_add_u32_e32 v38, 0xe00, v180
	s_lshl_b32 s35, s56, 28
	s_waitcnt lgkmcnt(1)
	v_add_f32_e32 v34, 0, v34
	v_add_f32_e32 v40, v34, v35
	ds_read2_b32 v[34:35], v38 offset1:224
	v_add_u32_e32 v38, 0x1500, v180
	ds_read2_b32 v[38:39], v38 offset1:224
	s_waitcnt lgkmcnt(2)
	v_add_f32_e32 v36, v40, v36
	v_add_f32_e32 v36, v36, v37
	s_waitcnt lgkmcnt(1)
	v_add_f32_e32 v34, v36, v34
	s_add_i32 s35, s35, 0xf0000000
	v_add_f32_e32 v34, v34, v35
	s_ashr_i32 s35, s35, 31
	s_waitcnt lgkmcnt(0)
	v_add_f32_e32 v34, v34, v38
	s_and_b32 s35, s35, 0x1800
	v_add_f32_e32 v34, v34, v39
	v_add_u32_e32 v35, s35, v232
	ds_write_b32 v35, v34 offset:896

.LBB1_145:
	v_lshl_add_u64 v[166:167], s[20:21], 4, v[154:155]
	global_load_dwordx4 v[154:157], v[166:167], off
	s_waitcnt lgkmcnt(5)
	v_mfma_f32_32x32x16_f16 v[34:49], v[122:125], v[50:53], v[2:17]
	ds_read_b128 v[244:247], v179 offset:33984
	v_cvt_pk_f16_f32 v172, v18, v19
	v_cvt_pk_f16_f32 v173, v20, v21
	s_waitcnt lgkmcnt(5)
	v_mfma_f32_32x32x16_f16 v[34:49], v[98:101], v[54:57], v[34:49]
	ds_read_b128 v[18:21], v179 offset:34016
	v_exp_f16_e64 v50, v172 clamp
	v_exp_f16_e64 v51, v173 clamp
	v_exp_f16_sdwa v50, v172 clamp dst_sel:WORD_1 dst_unused:UNUSED_PRESERVE src0_sel:WORD_1
	v_exp_f16_sdwa v51, v173 clamp dst_sel:WORD_1 dst_unused:UNUSED_PRESERVE src0_sel:WORD_1
	s_nop 0
	s_waitcnt lgkmcnt(5)
	v_mfma_f32_32x32x16_f16 v[34:49], v[114:117], v[58:61], v[34:49]
	ds_read_b128 v[248:251], v179 offset:34048
	v_pk_fma_f16 v51, v51, s55, v233 op_sel_hi:[1,0,0]
	v_pk_fma_f16 v50, v50, s55, v233 op_sel_hi:[1,0,0]
	v_pk_max_f16 v51, v173, v51
	v_pk_max_f16 v50, v172, v50
	s_waitcnt lgkmcnt(5)
	v_mfma_f32_32x32x16_f16 v[34:49], v[86:89], v[62:65], v[34:49]
	ds_read_b128 v[252:255], v179 offset:34080
	v_cvt_pk_f16_f32 v52, v22, v23
	v_cvt_pk_f16_f32 v53, v24, v25
	s_waitcnt lgkmcnt(5)
	v_mfma_f32_32x32x16_f16 v[34:49], v[126:129], v[168:171], v[34:49]
	ds_read_b128 v[22:25], v179 offset:34112
	v_exp_f16_e64 v54, v52 clamp
	v_exp_f16_e64 v55, v53 clamp
	v_exp_f16_sdwa v54, v52 clamp dst_sel:WORD_1 dst_unused:UNUSED_PRESERVE src0_sel:WORD_1
	v_exp_f16_sdwa v55, v53 clamp dst_sel:WORD_1 dst_unused:UNUSED_PRESERVE src0_sel:WORD_1
	s_nop 0
	s_waitcnt lgkmcnt(5)
	v_mfma_f32_32x32x16_f16 v[34:49], v[90:93], v[240:243], v[34:49]
	ds_read_b128 v[168:171], v179 offset:34144
	v_pk_fma_f16 v55, v55, s55, v233 op_sel_hi:[1,0,0]
	v_pk_fma_f16 v54, v54, s55, v233 op_sel_hi:[1,0,0]
	v_pk_max_f16 v53, v53, v55
	v_pk_max_f16 v52, v52, v54
	s_waitcnt lgkmcnt(5)
	v_mfma_f32_32x32x16_f16 v[34:49], v[118:121], v[244:247], v[34:49]
	ds_read_b128 v[240:243], v179 offset:34176
	v_cvt_pk_f16_f32 v172, v26, v27
	v_cvt_pk_f16_f32 v173, v28, v29
	v_mfma_f32_16x16x32_f16 v[62:65], v[70:73], v[50:53], 0
	s_waitcnt lgkmcnt(5)
	v_mfma_f32_32x32x16_f16 v[34:49], v[78:81], v[18:21], v[34:49]
	ds_read_b128 v[26:29], v179 offset:34208
	v_exp_f16_e64 v244, v172 clamp
	v_exp_f16_e64 v245, v173 clamp
	v_exp_f16_sdwa v244, v172 clamp dst_sel:WORD_1 dst_unused:UNUSED_PRESERVE src0_sel:WORD_1
	v_exp_f16_sdwa v245, v173 clamp dst_sel:WORD_1 dst_unused:UNUSED_PRESERVE src0_sel:WORD_1
	s_nop 0
	s_waitcnt lgkmcnt(5)
	v_mfma_f32_32x32x16_f16 v[34:49], v[102:105], v[248:251], v[34:49]
	ds_read_b128 v[18:21], v179 offset:34240
	v_pk_fma_f16 v245, v245, s55, v233 op_sel_hi:[1,0,0]
	s_nop 0
	v_pk_max_f16 v245, v173, v245
	v_pk_fma_f16 v173, v244, s55, v233 op_sel_hi:[1,0,0]
	s_nop 0
	v_pk_max_f16 v244, v172, v173
	s_waitcnt lgkmcnt(5)
	v_mfma_f32_32x32x16_f16 v[34:49], v[74:77], v[252:255], v[34:49]
	ds_read_b128 v[248:251], v179 offset:34272
	v_cvt_pk_f16_f32 v30, v30, v31
	v_cvt_pk_f16_f32 v31, v32, v33
	s_waitcnt lgkmcnt(5)
	v_mfma_f32_32x32x16_f16 v[34:49], v[106:109], v[22:25], v[34:49]
	v_exp_f16_e64 v32, v30 clamp
	v_exp_f16_e64 v33, v31 clamp
	v_exp_f16_sdwa v32, v30 clamp dst_sel:WORD_1 dst_unused:UNUSED_PRESERVE src0_sel:WORD_1
	v_exp_f16_sdwa v33, v31 clamp dst_sel:WORD_1 dst_unused:UNUSED_PRESERVE src0_sel:WORD_1
	s_nop 0
	s_waitcnt lgkmcnt(4)
	v_mfma_f32_32x32x16_f16 v[34:49], v[82:85], v[168:171], v[34:49]
	v_pk_fma_f16 v22, v33, s55, v233 op_sel_hi:[1,0,0]
	s_nop 0
	v_pk_max_f16 v247, v31, v22
	v_pk_fma_f16 v22, v32, s55, v233 op_sel_hi:[1,0,0]
	s_nop 0
	v_pk_max_f16 v246, v30, v22
	s_waitcnt lgkmcnt(3)
	v_mfma_f32_32x32x16_f16 v[34:49], v[110:113], v[240:243], v[34:49]
	s_waitcnt vmcnt(2)
	v_pk_add_f16 v24, v146, v158
	v_pk_add_f16 v25, v147, v159
	s_nop 0
	v_pk_mul_f16 v22, v160, v148 clamp
	v_pk_mul_f16 v23, v161, v149 clamp
	v_pk_max_f16 v22, v24, v22
	v_pk_max_f16 v23, v25, v23
	ds_write_b64 v189, v[22:23]
	v_mfma_f32_16x16x32_f16 v[62:65], v[66:69], v[244:247], v[62:65]
	s_waitcnt lgkmcnt(3)
	v_mfma_f32_32x32x16_f16 v[34:49], v[94:97], v[26:29], v[34:49]
	v_pk_add_f16 v24, v138, v158
	v_pk_add_f16 v25, v139, v159
	s_nop 0
	v_pk_mul_f16 v22, v160, v140 clamp
	v_pk_mul_f16 v23, v161, v141 clamp
	v_pk_max_f16 v22, v24, v22
	v_pk_max_f16 v23, v25, v23
	ds_write_b64 v189, v[22:23] offset:528
	s_waitcnt lgkmcnt(3)
	v_mfma_f32_32x32x16_f16 v[34:49], v[134:137], v[18:21], v[34:49]
	v_pk_add_f16 v24, v150, v158
	v_pk_add_f16 v25, v151, v159
	s_nop 0
	v_pk_mul_f16 v22, v160, v152 clamp
	v_pk_mul_f16 v23, v161, v153 clamp
	v_pk_max_f16 v22, v24, v22
	v_pk_max_f16 v23, v25, v23
	ds_write_b64 v189, v[22:23] offset:1056
	s_waitcnt lgkmcnt(3)
	v_mfma_f32_32x32x16_f16 v[34:49], v[130:133], v[248:251], v[34:49]
	v_pk_add_f16 v20, v142, v158
	v_pk_add_f16 v21, v143, v159
	s_nop 0
	v_pk_mul_f16 v18, v160, v144 clamp
	v_pk_mul_f16 v19, v161, v145 clamp
	v_pk_max_f16 v18, v20, v18
	v_pk_max_f16 v19, v21, v19
	ds_write_b64 v189, v[18:19] offset:1584
	ds_write2_b32 v201, v62, v63 offset1:1
	s_and_saveexec_b64 s[30:31], s[0:1]
	ds_write2_b32 v201, v64, v65 offset0:2 offset1:3
	s_or_b64 exec, exec, s[30:31]
	v_lshl_add_u64 v[166:167], s[20:21], 4, v[166:167]
	global_load_dwordx4 v[158:161], v[166:167], off
	ds_read_b128 v[50:53], v179 offset:50688
	ds_read_b128 v[54:57], v179 offset:50720
	ds_read_b128 v[58:61], v179 offset:50752
	ds_read_b128 v[62:65], v179 offset:50784
	ds_read_b128 v[168:171], v179 offset:50816
	ds_read_b128 v[240:243], v179 offset:50848
	s_waitcnt lgkmcnt(5)
	v_mfma_f32_32x32x16_f16 v[18:33], v[122:125], v[50:53], v[2:17]
	ds_read_b128 v[244:247], v179 offset:50880
	v_cvt_pk_f16_f32 v172, v34, v35
	v_cvt_pk_f16_f32 v173, v36, v37
	s_waitcnt lgkmcnt(5)
	v_mfma_f32_32x32x16_f16 v[18:33], v[98:101], v[54:57], v[18:33]
	ds_read_b128 v[34:37], v179 offset:50912
	v_exp_f16_e64 v50, v172 clamp
	v_exp_f16_e64 v51, v173 clamp
	v_exp_f16_sdwa v50, v172 clamp dst_sel:WORD_1 dst_unused:UNUSED_PRESERVE src0_sel:WORD_1
	v_exp_f16_sdwa v51, v173 clamp dst_sel:WORD_1 dst_unused:UNUSED_PRESERVE src0_sel:WORD_1
	s_nop 0
	s_waitcnt lgkmcnt(5)
	v_mfma_f32_32x32x16_f16 v[18:33], v[114:117], v[58:61], v[18:33]
	ds_read_b128 v[248:251], v179 offset:50944
	v_pk_fma_f16 v51, v51, s55, v233 op_sel_hi:[1,0,0]
	v_pk_fma_f16 v50, v50, s55, v233 op_sel_hi:[1,0,0]
	v_pk_max_f16 v51, v173, v51
	v_pk_max_f16 v50, v172, v50
	s_waitcnt lgkmcnt(5)
	v_mfma_f32_32x32x16_f16 v[18:33], v[86:89], v[62:65], v[18:33]
	ds_read_b128 v[252:255], v179 offset:50976
	v_cvt_pk_f16_f32 v52, v38, v39
	v_cvt_pk_f16_f32 v53, v40, v41
	s_waitcnt lgkmcnt(5)
	v_mfma_f32_32x32x16_f16 v[18:33], v[126:129], v[168:171], v[18:33]
	ds_read_b128 v[38:41], v179 offset:51008
	v_exp_f16_e64 v54, v52 clamp
	v_exp_f16_e64 v55, v53 clamp
	v_exp_f16_sdwa v54, v52 clamp dst_sel:WORD_1 dst_unused:UNUSED_PRESERVE src0_sel:WORD_1
	v_exp_f16_sdwa v55, v53 clamp dst_sel:WORD_1 dst_unused:UNUSED_PRESERVE src0_sel:WORD_1
	s_nop 0
	s_waitcnt lgkmcnt(5)
	v_mfma_f32_32x32x16_f16 v[18:33], v[90:93], v[240:243], v[18:33]
	ds_read_b128 v[168:171], v179 offset:51040
	v_pk_fma_f16 v55, v55, s55, v233 op_sel_hi:[1,0,0]
	v_pk_fma_f16 v54, v54, s55, v233 op_sel_hi:[1,0,0]
	v_pk_max_f16 v53, v53, v55
	v_pk_max_f16 v52, v52, v54
	s_waitcnt lgkmcnt(5)
	v_mfma_f32_32x32x16_f16 v[18:33], v[118:121], v[244:247], v[18:33]
	ds_read_b128 v[240:243], v179 offset:51072
	v_cvt_pk_f16_f32 v172, v42, v43
	v_cvt_pk_f16_f32 v173, v44, v45
	v_mfma_f32_16x16x32_f16 v[62:65], v[70:73], v[50:53], 0
	s_waitcnt lgkmcnt(5)
	v_mfma_f32_32x32x16_f16 v[18:33], v[78:81], v[34:37], v[18:33]
	ds_read_b128 v[42:45], v179 offset:51104
	v_exp_f16_e64 v244, v172 clamp
	v_exp_f16_e64 v245, v173 clamp
	v_exp_f16_sdwa v244, v172 clamp dst_sel:WORD_1 dst_unused:UNUSED_PRESERVE src0_sel:WORD_1
	v_exp_f16_sdwa v245, v173 clamp dst_sel:WORD_1 dst_unused:UNUSED_PRESERVE src0_sel:WORD_1
	s_nop 0
	s_waitcnt lgkmcnt(5)
	v_mfma_f32_32x32x16_f16 v[18:33], v[102:105], v[248:251], v[18:33]
	ds_read_b128 v[34:37], v179 offset:51136
	v_pk_fma_f16 v245, v245, s55, v233 op_sel_hi:[1,0,0]
	s_nop 0
	v_pk_max_f16 v245, v173, v245
	v_pk_fma_f16 v173, v244, s55, v233 op_sel_hi:[1,0,0]
	s_nop 0
	v_pk_max_f16 v244, v172, v173
	s_waitcnt lgkmcnt(5)
	v_mfma_f32_32x32x16_f16 v[18:33], v[74:77], v[252:255], v[18:33]
	ds_read_b128 v[248:251], v179 offset:51168
	v_cvt_pk_f16_f32 v46, v46, v47
	v_cvt_pk_f16_f32 v47, v48, v49
	s_waitcnt lgkmcnt(5)
	v_mfma_f32_32x32x16_f16 v[18:33], v[106:109], v[38:41], v[18:33]
	v_exp_f16_e64 v48, v46 clamp
	v_exp_f16_e64 v49, v47 clamp
	v_exp_f16_sdwa v48, v46 clamp dst_sel:WORD_1 dst_unused:UNUSED_PRESERVE src0_sel:WORD_1
	v_exp_f16_sdwa v49, v47 clamp dst_sel:WORD_1 dst_unused:UNUSED_PRESERVE src0_sel:WORD_1
	s_nop 0
	s_waitcnt lgkmcnt(4)
	v_mfma_f32_32x32x16_f16 v[18:33], v[82:85], v[168:171], v[18:33]
	v_pk_fma_f16 v38, v49, s55, v233 op_sel_hi:[1,0,0]
	s_nop 0
	v_pk_max_f16 v247, v47, v38
	v_pk_fma_f16 v38, v48, s55, v233 op_sel_hi:[1,0,0]
	s_nop 0
	v_pk_max_f16 v246, v46, v38
	s_waitcnt lgkmcnt(3)
	v_mfma_f32_32x32x16_f16 v[18:33], v[110:113], v[240:243], v[18:33]
	s_waitcnt vmcnt(2)
	v_pk_add_f16 v40, v146, v162
	v_pk_add_f16 v41, v147, v163
	s_nop 0
	v_pk_mul_f16 v38, v164, v148 clamp
	v_pk_mul_f16 v39, v165, v149 clamp
	v_pk_max_f16 v38, v40, v38
	v_pk_max_f16 v39, v41, v39
	ds_write_b64 v189, v[38:39] offset:16896
	v_mfma_f32_16x16x32_f16 v[62:65], v[66:69], v[244:247], v[62:65]
	s_waitcnt lgkmcnt(3)
	v_mfma_f32_32x32x16_f16 v[18:33], v[94:97], v[42:45], v[18:33]
	v_pk_add_f16 v40, v138, v162
	v_pk_add_f16 v41, v139, v163
	s_nop 0
	v_pk_mul_f16 v38, v164, v140 clamp
	v_pk_mul_f16 v39, v165, v141 clamp
	v_pk_max_f16 v38, v40, v38
	v_pk_max_f16 v39, v41, v39
	ds_write_b64 v189, v[38:39] offset:17424
	s_waitcnt lgkmcnt(3)
	v_mfma_f32_32x32x16_f16 v[18:33], v[134:137], v[34:37], v[18:33]
	v_pk_add_f16 v40, v150, v162
	v_pk_add_f16 v41, v151, v163
	s_nop 0
	v_pk_mul_f16 v38, v164, v152 clamp
	v_pk_mul_f16 v39, v165, v153 clamp
	v_pk_max_f16 v38, v40, v38
	v_pk_max_f16 v39, v41, v39
	ds_write_b64 v189, v[38:39] offset:17952
	s_waitcnt lgkmcnt(3)
	v_mfma_f32_32x32x16_f16 v[18:33], v[130:133], v[248:251], v[18:33]
	v_pk_add_f16 v36, v142, v162
	v_pk_add_f16 v37, v143, v163
	s_nop 0
	v_pk_mul_f16 v34, v164, v144 clamp
	v_pk_mul_f16 v35, v165, v145 clamp
	v_pk_max_f16 v34, v36, v34
	v_pk_max_f16 v35, v37, v35
	ds_write_b64 v189, v[34:35] offset:18480
	ds_write2_b32 v211, v62, v63 offset1:1
	s_and_saveexec_b64 s[30:31], s[0:1]
	ds_write2_b32 v211, v64, v65 offset0:2 offset1:3
	s_or_b64 exec, exec, s[30:31]
	s_add_i32 s35, s34, 1
	s_add_i32 s34, s56, 8
	s_cmp_eq_u32 s56, 8
	s_cselect_b64 vcc, -1, 0
	s_and_b64 s[30:31], vcc, exec
	v_lshl_add_u64 v[34:35], s[20:21], 4, v[166:167]
	s_cselect_b32 s20, s44, s20
	s_add_i32 s35, s35, 1
	s_and_b64 s[26:27], exec, s[26:27]
	s_cselect_b32 s30, s51, s35
	s_sub_i32 s26, 0x7e, s30
	s_mul_i32 s26, s26, 6
	s_ashr_i32 s27, s26, 31
	s_add_u32 s26, s28, s26
	s_addc_u32 s27, s29, s27
	s_add_i32 s31, s30, 1
	s_add_i32 s48, s48, 2
	s_add_i32 s54, s54, 16
	v_cndmask_b32_e32 v169, v35, v175, vcc
	v_cndmask_b32_e32 v168, v34, v174, vcc
	s_cmp_eq_u32 s34, 32
	s_waitcnt lgkmcnt(0)
	s_barrier
	s_cbranch_scc1 .LBB1_155
	ds_read_b128 v[50:53], v179
	ds_read_b128 v[54:57], v179 offset:32
	ds_read_b128 v[58:61], v179 offset:64
	ds_read_b128 v[62:65], v179 offset:96
	ds_read_b128 v[170:173], v179 offset:128
	ds_read_b128 v[240:243], v179 offset:160
	s_mov_b32 s56, s34
	s_and_b64 vcc, exec, s[8:9]
	s_cbranch_vccz .LBB1_42
	s_branch .LBB1_50
.LBB1_155:
	ds_read_b128 v[50:53], v179
	ds_read_b128 v[54:57], v179 offset:32
	ds_read_b128 v[58:61], v179 offset:64
	ds_read_b128 v[62:65], v179 offset:96
	ds_read_b128 v[162:165], v179 offset:128
	ds_read_b128 v[166:169], v179 offset:160
	s_and_b64 vcc, exec, s[24:25]
	s_cbranch_vccz .LBB1_164
	s_cmp_lg_u32 s41, 0
	s_cbranch_scc0 .LBB1_160
	s_and_saveexec_b64 s[12:13], s[6:7]
	s_cbranch_execz .LBB1_159
	ds_read2_b32 v[34:35], v200 offset1:224
	v_add_u32_e32 v36, 0x700, v200
	v_add_u32_e32 v38, 0xe00, v200
	ds_read2_b32 v[36:37], v36 offset1:224
	ds_read2_b32 v[38:39], v38 offset1:224
	s_waitcnt lgkmcnt(2)
	v_add_f32_e32 v34, 0, v34
	v_add_f32_e32 v40, v34, v35
	v_add_u32_e32 v34, 0x1500, v200
	ds_read2_b32 v[34:35], v34 offset1:224
	s_waitcnt lgkmcnt(2)
	v_add_f32_e32 v36, v40, v36
	v_add_f32_e32 v36, v36, v37
	s_waitcnt lgkmcnt(1)
	v_add_f32_e32 v36, v36, v38
	v_add_f32_e32 v36, v36, v39
	s_waitcnt lgkmcnt(0)
	v_add_f32_e32 v34, v36, v34
	v_add_f32_e32 v34, v34, v35
	v_mov_b32_e32 v35, 0x19080
	v_lshl_add_u32 v35, v177, 2, v35
	ds_write_b32 v35, v34

.LBB1_173:
	s_waitcnt lgkmcnt(5)
	v_mfma_f32_32x32x16_f16 v[34:49], v[122:125], v[50:53], v[2:17]
	ds_read_b128 v[170:173], v179 offset:192
	v_cvt_pk_f16_f32 v174, v18, v19
	v_cvt_pk_f16_f32 v175, v20, v21
	s_waitcnt lgkmcnt(5)
	v_mfma_f32_32x32x16_f16 v[34:49], v[98:101], v[54:57], v[34:49]
	ds_read_b128 v[18:21], v179 offset:224
	v_exp_f16_e64 v50, v174 clamp
	v_exp_f16_e64 v51, v175 clamp
	v_exp_f16_sdwa v50, v174 clamp dst_sel:WORD_1 dst_unused:UNUSED_PRESERVE src0_sel:WORD_1
	v_exp_f16_sdwa v51, v175 clamp dst_sel:WORD_1 dst_unused:UNUSED_PRESERVE src0_sel:WORD_1
	s_nop 0
	s_waitcnt lgkmcnt(5)
	v_mfma_f32_32x32x16_f16 v[34:49], v[114:117], v[58:61], v[34:49]
	ds_read_b128 v[230:233], v179 offset:256
	s_movk_i32 s20, 0x3dc5
	v_mov_b32_e32 v199, 0xbdc5
	v_pk_fma_f16 v51, v51, s20, v199 op_sel_hi:[1,0,0]
	v_pk_fma_f16 v50, v50, s20, v199 op_sel_hi:[1,0,0]
	v_pk_max_f16 v51, v175, v51
	v_pk_max_f16 v50, v174, v50
	s_waitcnt lgkmcnt(5)
	v_mfma_f32_32x32x16_f16 v[34:49], v[86:89], v[62:65], v[34:49]
	ds_read_b128 v[234:237], v179 offset:288
	v_cvt_pk_f16_f32 v52, v22, v23
	v_cvt_pk_f16_f32 v53, v24, v25
	s_waitcnt lgkmcnt(5)
	v_mfma_f32_32x32x16_f16 v[34:49], v[126:129], v[162:165], v[34:49]
	ds_read_b128 v[22:25], v179 offset:320
	v_exp_f16_e64 v54, v52 clamp
	v_exp_f16_e64 v55, v53 clamp
	v_exp_f16_sdwa v54, v52 clamp dst_sel:WORD_1 dst_unused:UNUSED_PRESERVE src0_sel:WORD_1
	v_exp_f16_sdwa v55, v53 clamp dst_sel:WORD_1 dst_unused:UNUSED_PRESERVE src0_sel:WORD_1
	s_nop 0
	s_waitcnt lgkmcnt(5)
	v_mfma_f32_32x32x16_f16 v[34:49], v[90:93], v[166:169], v[34:49]
	ds_read_b128 v[162:165], v179 offset:352
	v_pk_fma_f16 v55, v55, s20, v199 op_sel_hi:[1,0,0]
	v_pk_fma_f16 v54, v54, s20, v199 op_sel_hi:[1,0,0]
	v_pk_max_f16 v53, v53, v55
	v_pk_max_f16 v52, v52, v54
	s_waitcnt lgkmcnt(5)
	v_mfma_f32_32x32x16_f16 v[34:49], v[118:121], v[170:173], v[34:49]
	ds_read_b128 v[166:169], v179 offset:384
	v_cvt_pk_f16_f32 v170, v26, v27
	v_cvt_pk_f16_f32 v171, v28, v29
	v_mfma_f32_16x16x32_f16 v[62:65], v[70:73], v[50:53], 0
	s_waitcnt lgkmcnt(5)
	v_mfma_f32_32x32x16_f16 v[34:49], v[78:81], v[18:21], v[34:49]
	ds_read_b128 v[26:29], v179 offset:416
	v_exp_f16_e64 v172, v170 clamp
	v_exp_f16_e64 v173, v171 clamp
	v_exp_f16_sdwa v172, v170 clamp dst_sel:WORD_1 dst_unused:UNUSED_PRESERVE src0_sel:WORD_1
	v_exp_f16_sdwa v173, v171 clamp dst_sel:WORD_1 dst_unused:UNUSED_PRESERVE src0_sel:WORD_1
	s_nop 0
	s_waitcnt lgkmcnt(5)
	v_mfma_f32_32x32x16_f16 v[34:49], v[102:105], v[230:233], v[34:49]
	ds_read_b128 v[18:21], v179 offset:448
	v_pk_fma_f16 v173, v173, s20, v199 op_sel_hi:[1,0,0]
	v_pk_fma_f16 v172, v172, s20, v199 op_sel_hi:[1,0,0]
	v_pk_max_f16 v171, v171, v173
	v_pk_max_f16 v170, v170, v172
	s_waitcnt lgkmcnt(5)
	v_mfma_f32_32x32x16_f16 v[34:49], v[74:77], v[234:237], v[34:49]
	ds_read_b128 v[230:233], v179 offset:480
	v_cvt_pk_f16_f32 v30, v30, v31
	v_cvt_pk_f16_f32 v31, v32, v33
	s_waitcnt lgkmcnt(5)
	v_mfma_f32_32x32x16_f16 v[34:49], v[106:109], v[22:25], v[34:49]
	v_exp_f16_e64 v32, v30 clamp
	v_exp_f16_e64 v33, v31 clamp
	v_exp_f16_sdwa v32, v30 clamp dst_sel:WORD_1 dst_unused:UNUSED_PRESERVE src0_sel:WORD_1
	v_exp_f16_sdwa v33, v31 clamp dst_sel:WORD_1 dst_unused:UNUSED_PRESERVE src0_sel:WORD_1
	s_nop 0
	s_waitcnt lgkmcnt(4)
	v_mfma_f32_32x32x16_f16 v[34:49], v[82:85], v[162:165], v[34:49]
	v_pk_fma_f16 v22, v33, s20, v199 op_sel_hi:[1,0,0]
	s_nop 0
	v_pk_max_f16 v173, v31, v22
	v_pk_fma_f16 v22, v32, s20, v199 op_sel_hi:[1,0,0]
	s_nop 0
	v_pk_max_f16 v172, v30, v22
	s_waitcnt lgkmcnt(3)
	v_mfma_f32_32x32x16_f16 v[34:49], v[110:113], v[166:169], v[34:49]
	s_waitcnt vmcnt(1)
	v_pk_add_f16 v24, v146, v154
	v_pk_add_f16 v25, v147, v155
	s_nop 0
	v_pk_mul_f16 v22, v156, v148 clamp
	v_pk_mul_f16 v23, v157, v149 clamp
	v_pk_max_f16 v22, v24, v22
	v_pk_max_f16 v23, v25, v23
	ds_write_b64 v189, v[22:23] offset:33792
	v_mfma_f32_16x16x32_f16 v[62:65], v[66:69], v[170:173], v[62:65]
	s_waitcnt lgkmcnt(3)
	v_mfma_f32_32x32x16_f16 v[34:49], v[94:97], v[26:29], v[34:49]
	v_pk_add_f16 v24, v138, v154
	v_pk_add_f16 v25, v139, v155
	s_nop 0
	v_pk_mul_f16 v22, v156, v140 clamp
	v_pk_mul_f16 v23, v157, v141 clamp
	v_pk_max_f16 v22, v24, v22
	v_pk_max_f16 v23, v25, v23
	ds_write_b64 v189, v[22:23] offset:34320
	s_waitcnt lgkmcnt(3)
	v_mfma_f32_32x32x16_f16 v[34:49], v[134:137], v[18:21], v[34:49]
	v_pk_add_f16 v24, v150, v154
	v_pk_add_f16 v25, v151, v155
	s_nop 0
	v_pk_mul_f16 v22, v156, v152 clamp
	v_pk_mul_f16 v23, v157, v153 clamp
	v_pk_max_f16 v22, v24, v22
	v_pk_max_f16 v23, v25, v23
	ds_write_b64 v189, v[22:23] offset:34848
	s_waitcnt lgkmcnt(3)
	v_mfma_f32_32x32x16_f16 v[34:49], v[130:133], v[230:233], v[34:49]
	v_pk_add_f16 v20, v142, v154
	v_pk_add_f16 v21, v143, v155
	s_nop 0
	v_pk_mul_f16 v18, v156, v144 clamp
	v_pk_mul_f16 v19, v157, v145 clamp
	v_pk_max_f16 v18, v20, v18
	v_pk_max_f16 v19, v21, v19
	ds_write_b64 v189, v[18:19] offset:35376
	ds_write2_b32 v229, v62, v63 offset1:1
	s_and_saveexec_b64 s[20:21], s[0:1]
	ds_write2_b32 v229, v64, v65 offset0:2 offset1:3
	s_or_b64 exec, exec, s[20:21]
	ds_read_b128 v[50:53], v179 offset:16896
	ds_read_b128 v[54:57], v179 offset:16928
	ds_read_b128 v[58:61], v179 offset:16960
	ds_read_b128 v[62:65], v179 offset:16992
	ds_read_b128 v[154:157], v179 offset:17024
	ds_read_b128 v[162:165], v179 offset:17056
	s_waitcnt lgkmcnt(5)
	v_mfma_f32_32x32x16_f16 v[18:33], v[122:125], v[50:53], v[2:17]
	ds_read_b128 v[166:169], v179 offset:17088
	v_cvt_pk_f16_f32 v174, v34, v35
	v_cvt_pk_f16_f32 v175, v36, v37
	s_waitcnt lgkmcnt(5)
	v_mfma_f32_32x32x16_f16 v[18:33], v[98:101], v[54:57], v[18:33]
	ds_read_b128 v[34:37], v179 offset:17120
	v_exp_f16_e64 v50, v174 clamp
	v_exp_f16_e64 v51, v175 clamp
	v_exp_f16_sdwa v50, v174 clamp dst_sel:WORD_1 dst_unused:UNUSED_PRESERVE src0_sel:WORD_1
	v_exp_f16_sdwa v51, v175 clamp dst_sel:WORD_1 dst_unused:UNUSED_PRESERVE src0_sel:WORD_1
	s_nop 0
	s_waitcnt lgkmcnt(5)
	v_mfma_f32_32x32x16_f16 v[18:33], v[114:117], v[58:61], v[18:33]
	ds_read_b128 v[170:173], v179 offset:17152
	s_movk_i32 s20, 0x3dc5
	v_mov_b32_e32 v199, 0xbdc5
	v_pk_fma_f16 v51, v51, s20, v199 op_sel_hi:[1,0,0]
	v_pk_fma_f16 v50, v50, s20, v199 op_sel_hi:[1,0,0]
	v_pk_max_f16 v51, v175, v51
	v_pk_max_f16 v50, v174, v50
	s_waitcnt lgkmcnt(5)
	v_mfma_f32_32x32x16_f16 v[18:33], v[86:89], v[62:65], v[18:33]
	ds_read_b128 v[228:231], v179 offset:17184
	v_cvt_pk_f16_f32 v52, v38, v39
	v_cvt_pk_f16_f32 v53, v40, v41
	s_waitcnt lgkmcnt(5)
	v_mfma_f32_32x32x16_f16 v[18:33], v[126:129], v[154:157], v[18:33]
	ds_read_b128 v[38:41], v179 offset:17216
	v_exp_f16_e64 v54, v52 clamp
	v_exp_f16_e64 v55, v53 clamp
	v_exp_f16_sdwa v54, v52 clamp dst_sel:WORD_1 dst_unused:UNUSED_PRESERVE src0_sel:WORD_1
	v_exp_f16_sdwa v55, v53 clamp dst_sel:WORD_1 dst_unused:UNUSED_PRESERVE src0_sel:WORD_1
	s_nop 0
	s_waitcnt lgkmcnt(5)
	v_mfma_f32_32x32x16_f16 v[18:33], v[90:93], v[162:165], v[18:33]
	ds_read_b128 v[154:157], v179 offset:17248
	v_pk_fma_f16 v55, v55, s20, v199 op_sel_hi:[1,0,0]
	v_pk_fma_f16 v54, v54, s20, v199 op_sel_hi:[1,0,0]
	v_pk_max_f16 v53, v53, v55
	v_pk_max_f16 v52, v52, v54
	s_waitcnt lgkmcnt(5)
	v_mfma_f32_32x32x16_f16 v[18:33], v[118:121], v[166:169], v[18:33]
	ds_read_b128 v[162:165], v179 offset:17280
	v_cvt_pk_f16_f32 v166, v42, v43
	v_cvt_pk_f16_f32 v167, v44, v45
	v_mfma_f32_16x16x32_f16 v[62:65], v[70:73], v[50:53], 0
	s_waitcnt lgkmcnt(5)
	v_mfma_f32_32x32x16_f16 v[18:33], v[78:81], v[34:37], v[18:33]
	ds_read_b128 v[42:45], v179 offset:17312
	v_exp_f16_e64 v168, v166 clamp
	v_exp_f16_e64 v169, v167 clamp
	v_exp_f16_sdwa v168, v166 clamp dst_sel:WORD_1 dst_unused:UNUSED_PRESERVE src0_sel:WORD_1
	v_exp_f16_sdwa v169, v167 clamp dst_sel:WORD_1 dst_unused:UNUSED_PRESERVE src0_sel:WORD_1
	s_nop 0
	s_waitcnt lgkmcnt(5)
	v_mfma_f32_32x32x16_f16 v[18:33], v[102:105], v[170:173], v[18:33]
	ds_read_b128 v[34:37], v179 offset:17344
	v_pk_fma_f16 v169, v169, s20, v199 op_sel_hi:[1,0,0]
	v_pk_fma_f16 v168, v168, s20, v199 op_sel_hi:[1,0,0]
	v_pk_max_f16 v167, v167, v169
	v_pk_max_f16 v166, v166, v168
	s_waitcnt lgkmcnt(5)
	v_mfma_f32_32x32x16_f16 v[18:33], v[74:77], v[228:231], v[18:33]
	ds_read_b128 v[170:173], v179 offset:17376
	v_cvt_pk_f16_f32 v46, v46, v47
	v_cvt_pk_f16_f32 v47, v48, v49
	s_waitcnt lgkmcnt(5)
	v_mfma_f32_32x32x16_f16 v[18:33], v[106:109], v[38:41], v[18:33]
	v_exp_f16_e64 v48, v46 clamp
	v_exp_f16_e64 v49, v47 clamp
	v_exp_f16_sdwa v48, v46 clamp dst_sel:WORD_1 dst_unused:UNUSED_PRESERVE src0_sel:WORD_1
	v_exp_f16_sdwa v49, v47 clamp dst_sel:WORD_1 dst_unused:UNUSED_PRESERVE src0_sel:WORD_1
	s_nop 0
	s_waitcnt lgkmcnt(4)
	v_mfma_f32_32x32x16_f16 v[18:33], v[82:85], v[154:157], v[18:33]
	v_pk_fma_f16 v38, v49, s20, v199 op_sel_hi:[1,0,0]
	s_nop 0
	v_pk_max_f16 v169, v47, v38
	v_pk_fma_f16 v38, v48, s20, v199 op_sel_hi:[1,0,0]
	s_nop 0
	v_pk_max_f16 v168, v46, v38
	s_waitcnt lgkmcnt(3)
	v_mfma_f32_32x32x16_f16 v[18:33], v[110:113], v[162:165], v[18:33]
	s_waitcnt vmcnt(0)
	v_pk_add_f16 v40, v146, v158
	v_pk_add_f16 v41, v147, v159
	s_nop 0
	v_pk_mul_f16 v38, v160, v148 clamp
	v_pk_mul_f16 v39, v161, v149 clamp
	v_pk_max_f16 v38, v40, v38
	v_pk_max_f16 v39, v41, v39
	ds_write_b64 v189, v[38:39] offset:50688
	v_mfma_f32_16x16x32_f16 v[62:65], v[66:69], v[166:169], v[62:65]
	s_waitcnt lgkmcnt(3)
	v_mfma_f32_32x32x16_f16 v[18:33], v[94:97], v[42:45], v[18:33]
	v_pk_add_f16 v40, v138, v158
	v_pk_add_f16 v41, v139, v159
	s_nop 0
	v_pk_mul_f16 v38, v160, v140 clamp
	v_pk_mul_f16 v39, v161, v141 clamp
	v_pk_max_f16 v38, v40, v38
	v_pk_max_f16 v39, v41, v39
	ds_write_b64 v189, v[38:39] offset:51216
	s_waitcnt lgkmcnt(3)
	v_mfma_f32_32x32x16_f16 v[18:33], v[134:137], v[34:37], v[18:33]
	v_pk_add_f16 v40, v150, v158
	v_pk_add_f16 v41, v151, v159
	s_nop 0
	v_pk_mul_f16 v38, v160, v152 clamp
	v_pk_mul_f16 v39, v161, v153 clamp
	v_pk_max_f16 v38, v40, v38
	v_pk_max_f16 v39, v41, v39
	ds_write_b64 v189, v[38:39] offset:51744
	s_waitcnt lgkmcnt(3)
	v_mfma_f32_32x32x16_f16 v[18:33], v[130:133], v[170:173], v[18:33]
	v_pk_add_f16 v36, v142, v158
	v_pk_add_f16 v37, v143, v159
	s_nop 0
	v_pk_mul_f16 v34, v160, v144 clamp
	v_pk_mul_f16 v35, v161, v145 clamp
	v_pk_max_f16 v34, v36, v34
	v_pk_max_f16 v35, v37, v35
	ds_write_b64 v189, v[34:35] offset:52272
	ds_write2_b32 v206, v62, v63 offset1:1
	s_and_saveexec_b64 s[20:21], s[0:1]
	ds_write2_b32 v206, v64, v65 offset0:2 offset1:3
	s_or_b64 exec, exec, s[20:21]
	s_sub_i32 s20, 0x7c, s30
	s_mul_i32 s20, s20, 6
	s_ashr_i32 s21, s20, 31
	s_add_u32 s12, s12, s20
	s_addc_u32 s13, s13, s21
	s_and_b64 vcc, exec, s[8:9]
	s_waitcnt lgkmcnt(0)
	s_barrier
	s_cbranch_vccnz .LBB1_190
	s_cmp_lg_u32 s41, 0
	s_cbranch_scc0 .LBB1_186
	s_and_saveexec_b64 s[20:21], s[6:7]
	s_cbranch_execz .LBB1_185
	ds_read2_b32 v[34:35], v180 offset1:224
	v_add_u32_e32 v36, 0x700, v180
	v_add_u32_e32 v38, 0xe00, v180
	ds_read2_b32 v[36:37], v36 offset1:224
	ds_read2_b32 v[38:39], v38 offset1:224
	s_waitcnt lgkmcnt(2)
	v_add_f32_e32 v34, 0, v34
	v_add_f32_e32 v40, v34, v35
	v_add_u32_e32 v34, 0x1500, v180
	ds_read2_b32 v[34:35], v34 offset1:224
	s_waitcnt lgkmcnt(2)
	v_add_f32_e32 v36, v40, v36
	v_add_f32_e32 v36, v36, v37
	s_waitcnt lgkmcnt(1)
	v_add_f32_e32 v36, v36, v38
	v_add_f32_e32 v36, v36, v39
	s_waitcnt lgkmcnt(0)
	v_add_f32_e32 v34, v36, v34
	v_add_f32_e32 v34, v34, v35
	v_mov_b32_e32 v35, 0x19180
	v_lshl_add_u32 v35, v177, 2, v35
	ds_write_b32 v35, v34

.LBB1_199:
	ds_read_b128 v[50:53], v179 offset:33792
	ds_read_b128 v[54:57], v179 offset:33824
	ds_read_b128 v[58:61], v179 offset:33856
	ds_read_b128 v[62:65], v179 offset:33888
	ds_read_b128 v[138:141], v179 offset:33920
	ds_read_b128 v[142:145], v179 offset:33952
	s_waitcnt lgkmcnt(5)
	v_mfma_f32_32x32x16_f16 v[34:49], v[122:125], v[50:53], v[2:17]
	ds_read_b128 v[146:149], v179 offset:33984
	v_cvt_pk_f16_f32 v154, v18, v19
	v_cvt_pk_f16_f32 v155, v20, v21
	s_waitcnt lgkmcnt(5)
	v_mfma_f32_32x32x16_f16 v[34:49], v[98:101], v[54:57], v[34:49]
	ds_read_b128 v[18:21], v179 offset:34016
	v_exp_f16_e64 v50, v154 clamp
	v_exp_f16_e64 v51, v155 clamp
	v_exp_f16_sdwa v50, v154 clamp dst_sel:WORD_1 dst_unused:UNUSED_PRESERVE src0_sel:WORD_1
	v_exp_f16_sdwa v51, v155 clamp dst_sel:WORD_1 dst_unused:UNUSED_PRESERVE src0_sel:WORD_1
	s_nop 0
	s_waitcnt lgkmcnt(5)
	v_mfma_f32_32x32x16_f16 v[34:49], v[114:117], v[58:61], v[34:49]
	ds_read_b128 v[150:153], v179 offset:34048
	s_movk_i32 s20, 0x3dc5
	v_mov_b32_e32 v158, 0xbdc5
	v_pk_fma_f16 v51, v51, s20, v158 op_sel_hi:[1,0,0]
	v_pk_fma_f16 v50, v50, s20, v158 op_sel_hi:[1,0,0]
	v_pk_max_f16 v51, v155, v51
	v_pk_max_f16 v50, v154, v50
	s_waitcnt lgkmcnt(5)
	v_mfma_f32_32x32x16_f16 v[34:49], v[86:89], v[62:65], v[34:49]
	ds_read_b128 v[154:157], v179 offset:34080
	v_cvt_pk_f16_f32 v52, v22, v23
	v_cvt_pk_f16_f32 v53, v24, v25
	s_waitcnt lgkmcnt(5)
	v_mfma_f32_32x32x16_f16 v[34:49], v[126:129], v[138:141], v[34:49]
	ds_read_b128 v[22:25], v179 offset:34112
	v_exp_f16_e64 v54, v52 clamp
	v_exp_f16_e64 v55, v53 clamp
	v_exp_f16_sdwa v54, v52 clamp dst_sel:WORD_1 dst_unused:UNUSED_PRESERVE src0_sel:WORD_1
	v_exp_f16_sdwa v55, v53 clamp dst_sel:WORD_1 dst_unused:UNUSED_PRESERVE src0_sel:WORD_1
	s_nop 0
	s_waitcnt lgkmcnt(5)
	v_mfma_f32_32x32x16_f16 v[34:49], v[90:93], v[142:145], v[34:49]
	ds_read_b128 v[138:141], v179 offset:34144
	v_pk_fma_f16 v55, v55, s20, v158 op_sel_hi:[1,0,0]
	v_pk_fma_f16 v54, v54, s20, v158 op_sel_hi:[1,0,0]
	v_pk_max_f16 v53, v53, v55
	v_pk_max_f16 v52, v52, v54
	s_waitcnt lgkmcnt(5)
	v_mfma_f32_32x32x16_f16 v[34:49], v[118:121], v[146:149], v[34:49]
	ds_read_b128 v[142:145], v179 offset:34176
	v_cvt_pk_f16_f32 v146, v26, v27
	v_cvt_pk_f16_f32 v147, v28, v29
	v_mfma_f32_16x16x32_f16 v[62:65], v[70:73], v[50:53], 0
	s_waitcnt lgkmcnt(5)
	v_mfma_f32_32x32x16_f16 v[34:49], v[78:81], v[18:21], v[34:49]
	ds_read_b128 v[26:29], v179 offset:34208
	v_exp_f16_e64 v148, v146 clamp
	v_exp_f16_e64 v149, v147 clamp
	v_exp_f16_sdwa v148, v146 clamp dst_sel:WORD_1 dst_unused:UNUSED_PRESERVE src0_sel:WORD_1
	v_exp_f16_sdwa v149, v147 clamp dst_sel:WORD_1 dst_unused:UNUSED_PRESERVE src0_sel:WORD_1
	s_nop 0
	s_waitcnt lgkmcnt(5)
	v_mfma_f32_32x32x16_f16 v[34:49], v[102:105], v[150:153], v[34:49]
	ds_read_b128 v[18:21], v179 offset:34240
	v_pk_fma_f16 v149, v149, s20, v158 op_sel_hi:[1,0,0]
	v_pk_fma_f16 v148, v148, s20, v158 op_sel_hi:[1,0,0]
	v_pk_max_f16 v147, v147, v149
	v_pk_max_f16 v146, v146, v148
	s_waitcnt lgkmcnt(5)
	v_mfma_f32_32x32x16_f16 v[34:49], v[74:77], v[154:157], v[34:49]
	ds_read_b128 v[150:153], v179 offset:34272
	v_cvt_pk_f16_f32 v30, v30, v31
	v_cvt_pk_f16_f32 v31, v32, v33
	s_waitcnt lgkmcnt(5)
	v_mfma_f32_32x32x16_f16 v[34:49], v[106:109], v[22:25], v[34:49]
	v_exp_f16_e64 v32, v30 clamp
	v_exp_f16_e64 v33, v31 clamp
	v_exp_f16_sdwa v32, v30 clamp dst_sel:WORD_1 dst_unused:UNUSED_PRESERVE src0_sel:WORD_1
	v_exp_f16_sdwa v33, v31 clamp dst_sel:WORD_1 dst_unused:UNUSED_PRESERVE src0_sel:WORD_1
	s_nop 0
	s_waitcnt lgkmcnt(4)
	v_mfma_f32_32x32x16_f16 v[34:49], v[82:85], v[138:141], v[34:49]
	v_pk_fma_f16 v22, v33, s20, v158 op_sel_hi:[1,0,0]
	s_nop 0
	v_pk_max_f16 v149, v31, v22
	v_pk_fma_f16 v22, v32, s20, v158 op_sel_hi:[1,0,0]
	s_nop 0
	v_pk_max_f16 v148, v30, v22
	s_waitcnt lgkmcnt(3)
	v_mfma_f32_32x32x16_f16 v[34:49], v[110:113], v[142:145], v[34:49]
	v_mfma_f32_16x16x32_f16 v[62:65], v[66:69], v[146:149], v[62:65]
	s_waitcnt lgkmcnt(2)
	v_mfma_f32_32x32x16_f16 v[34:49], v[94:97], v[26:29], v[34:49]
	s_waitcnt lgkmcnt(1)
	v_mfma_f32_32x32x16_f16 v[34:49], v[134:137], v[18:21], v[34:49]
	s_waitcnt lgkmcnt(0)
	v_mfma_f32_32x32x16_f16 v[34:49], v[130:133], v[150:153], v[34:49]
	s_nop 5
	ds_write2_b32 v201, v62, v63 offset1:1
	s_and_saveexec_b64 s[20:21], s[0:1]
	ds_write2_b32 v201, v64, v65 offset0:2 offset1:3
	s_or_b64 exec, exec, s[20:21]
	ds_read_b128 v[18:21], v179 offset:50688
	ds_read_b128 v[22:25], v179 offset:50720
	ds_read_b128 v[26:29], v179 offset:50752
	ds_read_b128 v[30:33], v179 offset:50784
	ds_read_b128 v[50:53], v179 offset:50816
	ds_read_b128 v[54:57], v179 offset:50848
	s_waitcnt lgkmcnt(5)
	v_mfma_f32_32x32x16_f16 v[2:17], v[122:125], v[18:21], v[2:17]
	ds_read_b128 v[58:61], v179 offset:50880
	v_cvt_pk_f16_f32 v138, v34, v35
	v_cvt_pk_f16_f32 v139, v36, v37
	s_waitcnt lgkmcnt(5)
	v_mfma_f32_32x32x16_f16 v[2:17], v[98:101], v[22:25], v[2:17]
	ds_read_b128 v[34:37], v179 offset:50912
	v_exp_f16_e64 v18, v138 clamp
	v_exp_f16_e64 v19, v139 clamp
	v_exp_f16_sdwa v18, v138 clamp dst_sel:WORD_1 dst_unused:UNUSED_PRESERVE src0_sel:WORD_1
	v_exp_f16_sdwa v19, v139 clamp dst_sel:WORD_1 dst_unused:UNUSED_PRESERVE src0_sel:WORD_1
	s_nop 0
	s_waitcnt lgkmcnt(5)
	v_mfma_f32_32x32x16_f16 v[2:17], v[114:117], v[26:29], v[2:17]
	ds_read_b128 v[62:65], v179 offset:50944
	s_movk_i32 s20, 0x3dc5
	v_mov_b32_e32 v122, 0xbdc5
	v_pk_fma_f16 v19, v19, s20, v122 op_sel_hi:[1,0,0]
	v_pk_fma_f16 v18, v18, s20, v122 op_sel_hi:[1,0,0]
	v_pk_max_f16 v19, v139, v19
	v_pk_max_f16 v18, v138, v18
	s_waitcnt lgkmcnt(5)
	v_mfma_f32_32x32x16_f16 v[2:17], v[86:89], v[30:33], v[2:17]
	ds_read_b128 v[98:101], v179 offset:50976
	v_cvt_pk_f16_f32 v20, v38, v39
	v_cvt_pk_f16_f32 v21, v40, v41
	s_waitcnt lgkmcnt(5)
	v_mfma_f32_32x32x16_f16 v[2:17], v[126:129], v[50:53], v[2:17]
	ds_read_b128 v[38:41], v179 offset:51008
	v_exp_f16_e64 v22, v20 clamp
	v_exp_f16_e64 v23, v21 clamp
	v_exp_f16_sdwa v22, v20 clamp dst_sel:WORD_1 dst_unused:UNUSED_PRESERVE src0_sel:WORD_1
	v_exp_f16_sdwa v23, v21 clamp dst_sel:WORD_1 dst_unused:UNUSED_PRESERVE src0_sel:WORD_1
	s_nop 0
	s_waitcnt lgkmcnt(5)
	v_mfma_f32_32x32x16_f16 v[2:17], v[90:93], v[54:57], v[2:17]
	ds_read_b128 v[50:53], v179 offset:51040
	v_pk_fma_f16 v23, v23, s20, v122 op_sel_hi:[1,0,0]
	v_pk_fma_f16 v22, v22, s20, v122 op_sel_hi:[1,0,0]
	v_pk_max_f16 v21, v21, v23
	v_pk_max_f16 v20, v20, v22
	s_waitcnt lgkmcnt(5)
	v_mfma_f32_32x32x16_f16 v[2:17], v[118:121], v[58:61], v[2:17]
	ds_read_b128 v[54:57], v179 offset:51072
	v_cvt_pk_f16_f32 v58, v42, v43
	v_cvt_pk_f16_f32 v59, v44, v45
	v_mfma_f32_16x16x32_f16 v[30:33], v[70:73], v[18:21], 0
	s_waitcnt lgkmcnt(5)
	v_mfma_f32_32x32x16_f16 v[2:17], v[78:81], v[34:37], v[2:17]
	ds_read_b128 v[42:45], v179 offset:51104
	v_exp_f16_e64 v60, v58 clamp
	v_exp_f16_e64 v61, v59 clamp
	v_exp_f16_sdwa v60, v58 clamp dst_sel:WORD_1 dst_unused:UNUSED_PRESERVE src0_sel:WORD_1
	v_exp_f16_sdwa v61, v59 clamp dst_sel:WORD_1 dst_unused:UNUSED_PRESERVE src0_sel:WORD_1
	s_nop 0
	s_waitcnt lgkmcnt(5)
	v_mfma_f32_32x32x16_f16 v[2:17], v[102:105], v[62:65], v[2:17]
	ds_read_b128 v[34:37], v179 offset:51136
	v_pk_fma_f16 v61, v61, s20, v122 op_sel_hi:[1,0,0]
	v_pk_fma_f16 v60, v60, s20, v122 op_sel_hi:[1,0,0]
	v_pk_max_f16 v59, v59, v61
	v_pk_max_f16 v58, v58, v60
	s_waitcnt lgkmcnt(5)
	v_mfma_f32_32x32x16_f16 v[2:17], v[74:77], v[98:101], v[2:17]
	ds_read_b128 v[62:65], v179 offset:51168
	v_cvt_pk_f16_f32 v46, v46, v47
	v_cvt_pk_f16_f32 v47, v48, v49
	s_waitcnt lgkmcnt(5)
	v_mfma_f32_32x32x16_f16 v[2:17], v[106:109], v[38:41], v[2:17]
	v_exp_f16_e64 v48, v46 clamp
	v_exp_f16_e64 v49, v47 clamp
	v_exp_f16_sdwa v48, v46 clamp dst_sel:WORD_1 dst_unused:UNUSED_PRESERVE src0_sel:WORD_1
	v_exp_f16_sdwa v49, v47 clamp dst_sel:WORD_1 dst_unused:UNUSED_PRESERVE src0_sel:WORD_1
	s_nop 0
	s_waitcnt lgkmcnt(4)
	v_mfma_f32_32x32x16_f16 v[2:17], v[82:85], v[50:53], v[2:17]
	v_pk_fma_f16 v38, v49, s20, v122 op_sel_hi:[1,0,0]
	s_nop 0
	v_pk_max_f16 v61, v47, v38
	v_pk_fma_f16 v38, v48, s20, v122 op_sel_hi:[1,0,0]
	s_nop 0
	v_pk_max_f16 v60, v46, v38
	s_waitcnt lgkmcnt(3)
	v_mfma_f32_32x32x16_f16 v[2:17], v[110:113], v[54:57], v[2:17]
	v_mfma_f32_16x16x32_f16 v[30:33], v[66:69], v[58:61], v[30:33]
	s_waitcnt lgkmcnt(2)
	v_mfma_f32_32x32x16_f16 v[2:17], v[94:97], v[42:45], v[2:17]
	s_waitcnt lgkmcnt(1)
	v_mfma_f32_32x32x16_f16 v[2:17], v[134:137], v[34:37], v[2:17]
	s_waitcnt lgkmcnt(0)
	v_mfma_f32_32x32x16_f16 v[2:17], v[130:133], v[62:65], v[2:17]
	s_nop 5
	ds_write2_b32 v211, v30, v31 offset1:1
	s_and_saveexec_b64 s[20:21], s[0:1]
	ds_write2_b32 v211, v32, v33 offset0:2 offset1:3
	s_or_b64 exec, exec, s[20:21]
	s_sub_i32 s20, 0x7a, s30
	s_mul_i32 s20, s20, 6
	s_ashr_i32 s21, s20, 31
	s_add_u32 s12, s12, s20
	s_addc_u32 s13, s13, s21
	s_and_b64 vcc, exec, s[8:9]
	s_waitcnt lgkmcnt(0)
	s_barrier
	s_cbranch_vccnz .LBB1_216
	s_cmp_lg_u32 s41, 0
	s_cbranch_scc0 .LBB1_212
	s_and_saveexec_b64 s[20:21], s[6:7]
	s_cbranch_execz .LBB1_211
	ds_read2_b32 v[18:19], v200 offset1:224
	v_add_u32_e32 v20, 0x700, v200
	v_add_u32_e32 v22, 0xe00, v200
	ds_read2_b32 v[20:21], v20 offset1:224
	ds_read2_b32 v[22:23], v22 offset1:224
	s_waitcnt lgkmcnt(2)
	v_add_f32_e32 v18, 0, v18
	v_add_f32_e32 v24, v18, v19
	v_add_u32_e32 v18, 0x1500, v200
	ds_read2_b32 v[18:19], v18 offset1:224
	s_waitcnt lgkmcnt(2)
	v_add_f32_e32 v20, v24, v20
	v_add_f32_e32 v20, v20, v21
	s_waitcnt lgkmcnt(1)
	v_add_f32_e32 v20, v20, v22
	v_add_f32_e32 v20, v20, v23
	s_waitcnt lgkmcnt(0)
	v_add_f32_e32 v18, v20, v18
	v_add_f32_e32 v18, v18, v19
	v_mov_b32_e32 v19, 0x19280
	v_lshl_add_u32 v19, v177, 2, v19
	ds_write_b32 v19, v18

.LBB1_225:
	v_cvt_pk_f16_f32 v2, v2, v3
	v_cvt_pk_f16_f32 v3, v4, v5
	v_exp_f16_e64 v4, v2 clamp
	v_exp_f16_e64 v5, v3 clamp
	v_exp_f16_sdwa v4, v2 clamp dst_sel:WORD_1 dst_unused:UNUSED_PRESERVE src0_sel:WORD_1
	v_exp_f16_sdwa v5, v3 clamp dst_sel:WORD_1 dst_unused:UNUSED_PRESERVE src0_sel:WORD_1
	s_nop 0
	s_movk_i32 s20, 0x3dc5
	v_mov_b32_e32 v34, 0xbdc5
	v_pk_fma_f16 v5, v5, s20, v34 op_sel_hi:[1,0,0]
	v_pk_fma_f16 v4, v4, s20, v34 op_sel_hi:[1,0,0]
	v_pk_max_f16 v3, v3, v5
	v_pk_max_f16 v2, v2, v4
	v_cvt_pk_f16_f32 v4, v6, v7
	v_cvt_pk_f16_f32 v5, v8, v9
	v_exp_f16_e64 v6, v4 clamp
	v_exp_f16_e64 v7, v5 clamp
	v_exp_f16_sdwa v6, v4 clamp dst_sel:WORD_1 dst_unused:UNUSED_PRESERVE src0_sel:WORD_1
	v_exp_f16_sdwa v7, v5 clamp dst_sel:WORD_1 dst_unused:UNUSED_PRESERVE src0_sel:WORD_1
	s_nop 0
	s_nop 0
	v_pk_fma_f16 v7, v7, s20, v34 op_sel_hi:[1,0,0]
	v_pk_fma_f16 v6, v6, s20, v34 op_sel_hi:[1,0,0]
	v_pk_max_f16 v5, v5, v7
	v_pk_max_f16 v4, v4, v6
	s_nop 1
	v_mfma_f32_16x16x32_f16 v[30:33], v[70:73], v[2:5], 0
	v_cvt_pk_f16_f32 v6, v10, v11
	v_cvt_pk_f16_f32 v7, v12, v13
	v_exp_f16_e64 v2, v6 clamp
	v_exp_f16_e64 v3, v7 clamp
	v_exp_f16_sdwa v2, v6 clamp dst_sel:WORD_1 dst_unused:UNUSED_PRESERVE src0_sel:WORD_1
	v_exp_f16_sdwa v3, v7 clamp dst_sel:WORD_1 dst_unused:UNUSED_PRESERVE src0_sel:WORD_1
	s_nop 0
	s_nop 0
	v_pk_fma_f16 v3, v3, s20, v34 op_sel_hi:[1,0,0]
	v_pk_fma_f16 v2, v2, s20, v34 op_sel_hi:[1,0,0]
	v_pk_max_f16 v3, v7, v3
	v_pk_max_f16 v2, v6, v2
	v_cvt_pk_f16_f32 v4, v14, v15
	v_cvt_pk_f16_f32 v5, v16, v17
	v_exp_f16_e64 v6, v4 clamp
	v_exp_f16_e64 v7, v5 clamp
	v_exp_f16_sdwa v6, v4 clamp dst_sel:WORD_1 dst_unused:UNUSED_PRESERVE src0_sel:WORD_1
	v_exp_f16_sdwa v7, v5 clamp dst_sel:WORD_1 dst_unused:UNUSED_PRESERVE src0_sel:WORD_1
	s_nop 0
	s_nop 0
	v_pk_fma_f16 v7, v7, s20, v34 op_sel_hi:[1,0,0]
	v_pk_fma_f16 v6, v6, s20, v34 op_sel_hi:[1,0,0]
	v_pk_max_f16 v5, v5, v7
	v_pk_max_f16 v4, v4, v6
	s_nop 1
	v_mfma_f32_16x16x32_f16 v[30:33], v[66:69], v[2:5], v[30:33]
	v_mul_lo_u32 v2, v178, 28
	v_lshlrev_b32_e32 v1, 2, v1
	s_mov_b32 s20, 0x15c00
	v_add3_u32 v1, v2, v1, s20
	s_nop 7
	ds_write2_b32 v1, v30, v31 offset1:1
	s_and_saveexec_b64 s[20:21], s[0:1]
	ds_write2_b32 v1, v32, v33 offset0:2 offset1:3
	s_or_b64 exec, exec, s[20:21]
	s_and_b64 vcc, exec, s[8:9]
	s_waitcnt lgkmcnt(0)
	s_barrier
	s_cbranch_vccnz .LBB1_234
	s_cmp_lg_u32 s41, 0
	s_cbranch_scc0 .LBB1_237
	s_and_saveexec_b64 s[0:1], s[6:7]
	s_cbranch_execz .LBB1_233
	ds_read2_b32 v[2:3], v180 offset1:224
	v_add_u32_e32 v1, 0x700, v180
	v_add_u32_e32 v6, 0xe00, v180
	ds_read2_b32 v[4:5], v1 offset1:224
	ds_read2_b32 v[6:7], v6 offset1:224
	s_waitcnt lgkmcnt(2)
	v_add_f32_e32 v1, 0, v2
	v_add_u32_e32 v2, 0x1500, v180
	v_add_f32_e32 v1, v1, v3
	ds_read2_b32 v[2:3], v2 offset1:224
	s_waitcnt lgkmcnt(2)
	v_add_f32_e32 v1, v1, v4
	v_add_f32_e32 v1, v1, v5
	s_waitcnt lgkmcnt(1)
	v_add_f32_e32 v1, v1, v6
	v_add_f32_e32 v1, v1, v7
	s_waitcnt lgkmcnt(0)
	v_add_f32_e32 v1, v1, v2
	v_mov_b32_e32 v2, 0x19380
	v_add_f32_e32 v1, v1, v3
	v_lshl_add_u32 v2, v177, 2, v2
	ds_write_b32 v2, v1
